# layer-1 LN1 and final RMSNorm rows (MoE slot gather) hand-written: all 8 rows of a wave requested at once, slots of 4 rows gathered per round trip
# speedup vs baseline: 1.0149x; 1.0086x over previous
; DI void add_slots(const Args& A, int tok, int lane, f32x4 (&v)[4]) {
;     const int* sel = (const int*)(A.ws + WS_SEL); const bf16* ys = (const bf16*)(A.ws + WS_YS);
;     const int b = tok / SEQ; const int mys = (lane < NE) ? sel[(size_t)tok * NE + lane] : -1;
;     unsigned m = (unsigned)__ballot(mys >= 0);
;     while (m) {
;         const uint2* p[4]; bool ok[4];
; #pragma unroll
;         for (int q = 0; q < 4; ++q) { ok[q] = m != 0u; const int e = ok[q] ? __builtin_ctz(m) : 0; m &= m - 1u; const int r = __shfl(mys, e);
; DI void phase_ln1(const Args& A, int l, int gw, int ngw, int lane) {
;     const float* xin = A.in[I_X]; const bf16* x1 = (const bf16*)(A.ws + WS_X1); bf16* x2 = (bf16*)(A.ws + WS_X2); bf16* hb = (bf16*)(A.ws + WS_HB);
;     f32x4 gg[4];
; #pragma unroll
;     for (int j = 0; j < 4; ++j) gg[j] = ((const f32x4*)(A.in[I_LN1G] + (size_t)l * DM) + lane)[64 * j];
;     for (int tok = gw; tok < NT; tok += 2 * ngw) {
;         const int tokb = tok + ngw; const bool hb2 = tokb < NT;
;         f32x4 va[4], vb[4];
;         if (l == 0) { load_row(xin + (size_t)tok * DM, lane, va); load_row(xin + (size_t)(hb2 ? tokb : tok) * DM, lane, vb); }
;         else { load_row_bf(x1 + (size_t)tok * DM, lane, va); load_row_bf(x1 + (size_t)(hb2 ? tokb : tok) * DM, lane, vb);
;             add_slots(A, tok, lane, va); add_slots(A, hb2 ? tokb : tok, lane, vb);
;             uint2* oa = (uint2*)(x2 + (size_t)tok * DM) + lane; uint2* ob = (uint2*)(x2 + (size_t)tokb * DM) + lane;
; #pragma unroll
;             for (int j = 0; j < 4; ++j) { uint2 w; w.x = pkbf(va[j][0], va[j][1]); w.y = pkbf(va[j][2], va[j][3]); oa[64 * j] = w;
;                 if (hb2) { uint2 u; u.x = pkbf(vb[j][0], vb[j][1]); u.y = pkbf(vb[j][2], vb[j][3]); ob[64 * j] = u; } } }
;         const float ra = row_rstd(va), rb = row_rstd(vb); uint2* o8a = (uint2*)(hb + (size_t)tok * DM) + lane; uint2* o8b = (uint2*)(hb + (size_t)tokb * DM) + lane;
; #pragma unroll
;         for (int j = 0; j < 4; ++j) { uint2 w; w.x = pkbf(va[j][0] * ra * gg[j][0], va[j][1] * ra * gg[j][1]); w.y = pkbf(va[j][2] * ra * gg[j][2], va[j][3] * ra * gg[j][3]); o8a[64 * j] = w;
;             if (hb2) { uint2 u; u.x = pkbf(vb[j][0] * rb * gg[j][0], vb[j][1] * rb * gg[j][1]); u.y = pkbf(vb[j][2] * rb * gg[j][2], vb[j][3] * rb * gg[j][3]); o8b[64 * j] = u; } }
;     }
.LBB0_1519:
	s_cmp_lt_i32 s10, 12
	s_cselect_b64 s[2:3], -1, 0
	s_and_b64 s[0:1], s[2:3], s[0:1]
	v_readlane_b32 s4, v235, 54
	v_readlane_b32 s5, v235, 55
	s_cmpk_lt_i32 s4, 0x4000
	s_cselect_b64 s[4:5], -1, 0
	v_writelane_b32 v234, s4, 42
	s_and_b64 s[0:1], s[0:1], s[4:5]
	s_andn2_b64 vcc, exec, s[0:1]
	v_writelane_b32 v234, s5, 43
	s_cbranch_vccnz .LBB0_1579
	s_cmpk_lg_i32 s50, 0x100
	s_cbranch_scc1 .Lrw1_orig
	s_waitcnt vmcnt(0) lgkmcnt(0)
	v_readlane_b32 s0, v235, 9
	v_readlane_b32 s1, v235, 10
	v_readlane_b32 s18, v235, 54
	v_readlane_b32 s20, v235, 21
	v_readlane_b32 s21, v235, 22
	v_lshlrev_b32_e32 v1, 3, v146
	v_lshlrev_b32_e32 v2, 2, v146
	v_lshlrev_b32_e32 v3, 4, v146
	v_xor_b32_e32 v4, 1, v146
	v_lshlrev_b32_e32 v4, 2, v4
	v_xor_b32_e32 v5, 2, v146
	v_lshlrev_b32_e32 v5, 2, v5
	v_xor_b32_e32 v6, 4, v146
	v_lshlrev_b32_e32 v6, 2, v6
	v_xor_b32_e32 v7, 8, v146
	v_lshlrev_b32_e32 v7, 2, v7
	v_xor_b32_e32 v8, 16, v146
	v_lshlrev_b32_e32 v8, 2, v8
	v_xor_b32_e32 v9, 32, v146
	v_lshlrev_b32_e32 v9, 2, v9
	v_mov_b32_e32 v171, 0x358637bd
	s_mov_b32 s39, 0x3a800000
	s_mov_b32 s40, 0x800000
	s_lshl_b32 s19, s18, 11
	s_add_u32 s4, s0, 0x22600000
	s_addc_u32 s5, s1, 0
	s_add_u32 s4, s4, s19
	s_addc_u32 s5, s5, 0
	s_lshl_b32 s34, s18, 6
	s_add_u32 s6, s0, 0x2c700000
	s_addc_u32 s7, s1, 0
	s_add_u32 s6, s6, s34
	s_addc_u32 s7, s7, 0
	s_add_u32 s12, s0, 0x3ba00000
	s_addc_u32 s13, s1, 0
	s_add_u32 s14, s0, 0x26600000
	s_addc_u32 s15, s1, 0
	s_add_u32 s14, s14, s19
	s_addc_u32 s15, s15, 0
	s_add_u32 s16, s0, 0x2a600000
	s_addc_u32 s17, s1, 0
	s_add_u32 s16, s16, s19
	s_addc_u32 s17, s17, 0
	s_add_u32 s20, s20, 0x1000
	s_addc_u32 s21, s21, 0
	v_mov_b32_e32 v10, -1
	v_mov_b32_e32 v11, -1
	v_mov_b32_e32 v12, -1
	v_mov_b32_e32 v13, -1
	v_mov_b32_e32 v14, -1
	v_mov_b32_e32 v15, -1
	v_mov_b32_e32 v16, -1
	v_mov_b32_e32 v17, -1
	s_mov_b64 exec, 0xffff
	s_mov_b64 s[34:35], s[6:7]
	global_load_dword v10, v2, s[34:35]
	s_add_u32 s34, s6, 0x20000
	s_addc_u32 s35, s7, 0
	global_load_dword v11, v2, s[34:35]
	s_add_u32 s34, s6, 0x40000
	s_addc_u32 s35, s7, 0
	global_load_dword v12, v2, s[34:35]
	s_add_u32 s34, s6, 0x60000
	s_addc_u32 s35, s7, 0
	global_load_dword v13, v2, s[34:35]
	s_add_u32 s34, s6, 0x80000
	s_addc_u32 s35, s7, 0
	global_load_dword v14, v2, s[34:35]
	s_add_u32 s34, s6, 0xa0000
	s_addc_u32 s35, s7, 0
	global_load_dword v15, v2, s[34:35]
	s_add_u32 s34, s6, 0xc0000
	s_addc_u32 s35, s7, 0
	global_load_dword v16, v2, s[34:35]
	s_add_u32 s34, s6, 0xe0000
	s_addc_u32 s35, s7, 0
	global_load_dword v17, v2, s[34:35]
	s_mov_b64 exec, -1
	s_mov_b64 s[34:35], s[4:5]
	global_load_dwordx2 v[34:35], v1, s[34:35]
	global_load_dwordx2 v[36:37], v1, s[34:35] offset:512
	global_load_dwordx2 v[38:39], v1, s[34:35] offset:1024
	global_load_dwordx2 v[40:41], v1, s[34:35] offset:1536
	s_add_u32 s34, s4, 0x400000
	s_addc_u32 s35, s5, 0
	global_load_dwordx2 v[42:43], v1, s[34:35]
	global_load_dwordx2 v[44:45], v1, s[34:35] offset:512
	global_load_dwordx2 v[46:47], v1, s[34:35] offset:1024
	global_load_dwordx2 v[48:49], v1, s[34:35] offset:1536
	s_add_u32 s34, s4, 0x800000
	s_addc_u32 s35, s5, 0
	global_load_dwordx2 v[50:51], v1, s[34:35]
	global_load_dwordx2 v[52:53], v1, s[34:35] offset:512
	global_load_dwordx2 v[54:55], v1, s[34:35] offset:1024
	global_load_dwordx2 v[56:57], v1, s[34:35] offset:1536
	s_add_u32 s34, s4, 0xc00000
	s_addc_u32 s35, s5, 0
	global_load_dwordx2 v[58:59], v1, s[34:35]
	global_load_dwordx2 v[60:61], v1, s[34:35] offset:512
	global_load_dwordx2 v[62:63], v1, s[34:35] offset:1024
	global_load_dwordx2 v[64:65], v1, s[34:35] offset:1536
	s_add_u32 s34, s4, 0x1000000
	s_addc_u32 s35, s5, 0
	global_load_dwordx2 v[66:67], v1, s[34:35]
	global_load_dwordx2 v[68:69], v1, s[34:35] offset:512
	global_load_dwordx2 v[70:71], v1, s[34:35] offset:1024
	global_load_dwordx2 v[72:73], v1, s[34:35] offset:1536
	s_add_u32 s34, s4, 0x1400000
	s_addc_u32 s35, s5, 0
	global_load_dwordx2 v[74:75], v1, s[34:35]
	global_load_dwordx2 v[76:77], v1, s[34:35] offset:512
	global_load_dwordx2 v[78:79], v1, s[34:35] offset:1024
	global_load_dwordx2 v[80:81], v1, s[34:35] offset:1536
	s_add_u32 s34, s4, 0x1800000
	s_addc_u32 s35, s5, 0
	global_load_dwordx2 v[82:83], v1, s[34:35]
	global_load_dwordx2 v[84:85], v1, s[34:35] offset:512
	global_load_dwordx2 v[86:87], v1, s[34:35] offset:1024
	global_load_dwordx2 v[88:89], v1, s[34:35] offset:1536
	s_add_u32 s34, s4, 0x1c00000
	s_addc_u32 s35, s5, 0
	global_load_dwordx2 v[90:91], v1, s[34:35]
	global_load_dwordx2 v[92:93], v1, s[34:35] offset:512
	global_load_dwordx2 v[94:95], v1, s[34:35] offset:1024
	global_load_dwordx2 v[96:97], v1, s[34:35] offset:1536
	global_load_dwordx4 v[18:21], v3, s[20:21]
	global_load_dwordx4 v[22:25], v3, s[20:21] offset:1024
	global_load_dwordx4 v[26:29], v3, s[20:21] offset:2048
	global_load_dwordx4 v[30:33], v3, s[20:21] offset:3072
	s_waitcnt vmcnt(36)
	v_cmp_le_i32_e64 s[66:67], 0, v10
	v_cmp_le_i32_e64 s[68:69], 0, v11
	v_cmp_le_i32_e64 s[70:71], 0, v12
	v_cmp_le_i32_e64 s[72:73], 0, v13
	v_cmp_le_i32_e64 s[74:75], 0, v14
	v_cmp_le_i32_e64 s[76:77], 0, v15
	v_cmp_le_i32_e64 s[78:79], 0, v16
	v_cmp_le_i32_e64 s[80:81], 0, v17
	s_nop 1
	s_mov_b32 s38, 1
.Lrw1_round0:
	s_mov_b32 s33, 0
	s_cmp_eq_u32 s66, 0
	s_cbranch_scc1 .Lrw1_i0_0
	s_ff1_i32_b32 s34, s66
	s_add_i32 s35, s66, -1
	s_and_b32 s66, s66, s35
	s_nop 1
	v_readlane_b32 s35, v10, s34
	s_lshl_b32 s34, s34, 22
	s_lshl_b32 s35, s35, 11
	s_add_u32 s34, s34, s35
	s_add_u32 s36, s12, s34
	s_addc_u32 s37, s13, 0
	global_load_dwordx2 v[98:99], v1, s[36:37]
	global_load_dwordx2 v[100:101], v1, s[36:37] offset:512
	global_load_dwordx2 v[102:103], v1, s[36:37] offset:1024
	global_load_dwordx2 v[104:105], v1, s[36:37] offset:1536
	s_bitset1_b32 s33, 0
; DI void add_slots(const Args& A, int tok, int lane, f32x4 (&v)[4]) {
;     ...
;     while (m) {
;         const uint2* p[4]; bool ok[4];
; #pragma unroll
;         for (int q = 0; q < 4; ++q) { ok[q] = m != 0u; const int e = ok[q] ? __builtin_ctz(m) : 0; m &= m - 1u; const int r = __shfl(mys, e);
;             p[q] = (const uint2*)(ys + (size_t)((e * NB + b) * CAP + (ok[q] ? r : 0)) * DM) + lane; }
;         uint2 w[4][4];
; #pragma unroll
;         for (int q = 0; q < 4; ++q) if (ok[q]) {
; #pragma unroll
;             for (int j = 0; j < 4; ++j) w[q][j] = p[q][64 * j]; }
.Lrw1_i0_0:
	s_cmp_eq_u32 s66, 0
	s_cbranch_scc1 .Lrw1_i0_1
	s_ff1_i32_b32 s34, s66
	s_add_i32 s35, s66, -1
	s_and_b32 s66, s66, s35
	s_nop 1
	v_readlane_b32 s35, v10, s34
	s_lshl_b32 s34, s34, 22
	s_lshl_b32 s35, s35, 11
	s_add_u32 s34, s34, s35
	s_add_u32 s36, s12, s34
	s_addc_u32 s37, s13, 0
	global_load_dwordx2 v[106:107], v1, s[36:37]
	global_load_dwordx2 v[108:109], v1, s[36:37] offset:512
	global_load_dwordx2 v[110:111], v1, s[36:37] offset:1024
	global_load_dwordx2 v[112:113], v1, s[36:37] offset:1536
	s_bitset1_b32 s33, 1
.Lrw1_i0_1:
	s_cmp_eq_u32 s68, 0
	s_cbranch_scc1 .Lrw1_i0_2
	s_ff1_i32_b32 s34, s68
	s_add_i32 s35, s68, -1
	s_and_b32 s68, s68, s35
	s_nop 1
	v_readlane_b32 s35, v11, s34
	s_lshl_b32 s34, s34, 22
	s_lshl_b32 s35, s35, 11
	s_add_u32 s34, s34, s35
	s_add_u32 s34, s34, 0x80000
	s_add_u32 s36, s12, s34
	s_addc_u32 s37, s13, 0
	global_load_dwordx2 v[114:115], v1, s[36:37]
	global_load_dwordx2 v[116:117], v1, s[36:37] offset:512
	global_load_dwordx2 v[118:119], v1, s[36:37] offset:1024
	global_load_dwordx2 v[148:149], v1, s[36:37] offset:1536
	s_bitset1_b32 s33, 2
.Lrw1_i0_2:
	s_cmp_eq_u32 s68, 0
	s_cbranch_scc1 .Lrw1_i0_3
	s_ff1_i32_b32 s34, s68
	s_add_i32 s35, s68, -1
	s_and_b32 s68, s68, s35
	s_nop 1
	v_readlane_b32 s35, v11, s34
	s_lshl_b32 s34, s34, 22
	s_lshl_b32 s35, s35, 11
	s_add_u32 s34, s34, s35
	s_add_u32 s34, s34, 0x80000
	s_add_u32 s36, s12, s34
	s_addc_u32 s37, s13, 0
	global_load_dwordx2 v[150:151], v1, s[36:37]
	global_load_dwordx2 v[152:153], v1, s[36:37] offset:512
	global_load_dwordx2 v[154:155], v1, s[36:37] offset:1024
	global_load_dwordx2 v[156:157], v1, s[36:37] offset:1536
	s_bitset1_b32 s33, 3
.Lrw1_i0_3:
	s_cmp_eq_u32 s70, 0
	s_cbranch_scc1 .Lrw1_i0_4
	s_ff1_i32_b32 s34, s70
	s_add_i32 s35, s70, -1
	s_and_b32 s70, s70, s35
	s_nop 1
	v_readlane_b32 s35, v12, s34
	s_lshl_b32 s34, s34, 22
	s_lshl_b32 s35, s35, 11
	s_add_u32 s34, s34, s35
	s_add_u32 s34, s34, 0x100000
	s_add_u32 s36, s12, s34
	s_addc_u32 s37, s13, 0
	global_load_dwordx2 v[158:159], v1, s[36:37]
	global_load_dwordx2 v[160:161], v1, s[36:37] offset:512
	global_load_dwordx2 v[162:163], v1, s[36:37] offset:1024
	global_load_dwordx2 v[164:165], v1, s[36:37] offset:1536
	s_bitset1_b32 s33, 4
.Lrw1_i0_4:
	s_cmp_eq_u32 s70, 0
	s_cbranch_scc1 .Lrw1_i0_5
	s_ff1_i32_b32 s34, s70
	s_add_i32 s35, s70, -1
	s_and_b32 s70, s70, s35
	s_nop 1
	v_readlane_b32 s35, v12, s34
	s_lshl_b32 s34, s34, 22
	s_lshl_b32 s35, s35, 11
	s_add_u32 s34, s34, s35
	s_add_u32 s34, s34, 0x100000
	s_add_u32 s36, s12, s34
	s_addc_u32 s37, s13, 0
	global_load_dwordx2 v[166:167], v1, s[36:37]
	global_load_dwordx2 v[168:169], v1, s[36:37] offset:512
	global_load_dwordx2 v[220:221], v1, s[36:37] offset:1024
	global_load_dwordx2 v[222:223], v1, s[36:37] offset:1536
	s_bitset1_b32 s33, 5
.Lrw1_i0_5:
	s_cmp_eq_u32 s72, 0
	s_cbranch_scc1 .Lrw1_i0_6
	s_ff1_i32_b32 s34, s72
	s_add_i32 s35, s72, -1
	s_and_b32 s72, s72, s35
	s_nop 1
	v_readlane_b32 s35, v13, s34
	s_lshl_b32 s34, s34, 22
	s_lshl_b32 s35, s35, 11
	s_add_u32 s34, s34, s35
	s_add_u32 s34, s34, 0x180000
	s_add_u32 s36, s12, s34
	s_addc_u32 s37, s13, 0
	global_load_dwordx2 v[224:225], v1, s[36:37]
	global_load_dwordx2 v[226:227], v1, s[36:37] offset:512
	global_load_dwordx2 v[228:229], v1, s[36:37] offset:1024
	global_load_dwordx2 v[230:231], v1, s[36:37] offset:1536
	s_bitset1_b32 s33, 6
.Lrw1_i0_6:
	s_cmp_eq_u32 s72, 0
	s_cbranch_scc1 .Lrw1_i0_7
	s_ff1_i32_b32 s34, s72
	s_add_i32 s35, s72, -1
	s_and_b32 s72, s72, s35
	s_nop 1
	v_readlane_b32 s35, v13, s34
	s_lshl_b32 s34, s34, 22
	s_lshl_b32 s35, s35, 11
	s_add_u32 s34, s34, s35
	s_add_u32 s34, s34, 0x180000
	s_add_u32 s36, s12, s34
	s_addc_u32 s37, s13, 0
	global_load_dwordx2 v[232:233], v1, s[36:37]
	global_load_dwordx2 v[140:141], v1, s[36:37] offset:512
	global_load_dwordx2 v[142:143], v1, s[36:37] offset:1024
	global_load_dwordx2 v[144:145], v1, s[36:37] offset:1536
	s_bitset1_b32 s33, 7
.Lrw1_i0_7:
	s_waitcnt vmcnt(0)
	s_cmp_eq_u32 s38, 0
	s_cbranch_scc1 .Lrw1_nounp0
	v_lshlrev_b32_e32 v172, 16, v34
	v_and_b32_e32 v173, 0xffff0000, v34
	v_lshlrev_b32_e32 v174, 16, v35
	v_and_b32_e32 v175, 0xffff0000, v35
	v_lshlrev_b32_e32 v176, 16, v36
	v_and_b32_e32 v177, 0xffff0000, v36
	v_lshlrev_b32_e32 v178, 16, v37
	v_and_b32_e32 v179, 0xffff0000, v37
	v_lshlrev_b32_e32 v180, 16, v38
	v_and_b32_e32 v181, 0xffff0000, v38
	v_lshlrev_b32_e32 v182, 16, v39
	v_and_b32_e32 v183, 0xffff0000, v39
	v_lshlrev_b32_e32 v184, 16, v40
	v_and_b32_e32 v185, 0xffff0000, v40
	v_lshlrev_b32_e32 v186, 16, v41
	v_and_b32_e32 v187, 0xffff0000, v41
	v_lshlrev_b32_e32 v188, 16, v42
	v_and_b32_e32 v189, 0xffff0000, v42
	v_lshlrev_b32_e32 v190, 16, v43
	v_and_b32_e32 v191, 0xffff0000, v43
	v_lshlrev_b32_e32 v192, 16, v44
	v_and_b32_e32 v193, 0xffff0000, v44
	v_lshlrev_b32_e32 v194, 16, v45
	v_and_b32_e32 v195, 0xffff0000, v45
	v_lshlrev_b32_e32 v196, 16, v46
	v_and_b32_e32 v197, 0xffff0000, v46
	v_lshlrev_b32_e32 v198, 16, v47
	v_and_b32_e32 v199, 0xffff0000, v47
	v_lshlrev_b32_e32 v200, 16, v48
	v_and_b32_e32 v201, 0xffff0000, v48
	v_lshlrev_b32_e32 v202, 16, v49
	v_and_b32_e32 v203, 0xffff0000, v49
	v_lshlrev_b32_e32 v204, 16, v50
	v_and_b32_e32 v205, 0xffff0000, v50
	v_lshlrev_b32_e32 v206, 16, v51
	v_and_b32_e32 v207, 0xffff0000, v51
	v_lshlrev_b32_e32 v208, 16, v52
	v_and_b32_e32 v209, 0xffff0000, v52
	v_lshlrev_b32_e32 v210, 16, v53
	v_and_b32_e32 v211, 0xffff0000, v53
	v_lshlrev_b32_e32 v212, 16, v54
	v_and_b32_e32 v213, 0xffff0000, v54
	v_lshlrev_b32_e32 v214, 16, v55
	v_and_b32_e32 v215, 0xffff0000, v55
	v_lshlrev_b32_e32 v216, 16, v56
	v_and_b32_e32 v217, 0xffff0000, v56
	v_lshlrev_b32_e32 v218, 16, v57
	v_and_b32_e32 v219, 0xffff0000, v57
	v_lshlrev_b32_e32 v236, 16, v58
	v_and_b32_e32 v237, 0xffff0000, v58
	v_lshlrev_b32_e32 v238, 16, v59
	v_and_b32_e32 v239, 0xffff0000, v59
	v_lshlrev_b32_e32 v240, 16, v60
	v_and_b32_e32 v241, 0xffff0000, v60
	v_lshlrev_b32_e32 v242, 16, v61
	v_and_b32_e32 v243, 0xffff0000, v61
	v_lshlrev_b32_e32 v244, 16, v62
	v_and_b32_e32 v245, 0xffff0000, v62
	v_lshlrev_b32_e32 v246, 16, v63
	v_and_b32_e32 v247, 0xffff0000, v63
	v_lshlrev_b32_e32 v248, 16, v64
	v_and_b32_e32 v249, 0xffff0000, v64
	v_lshlrev_b32_e32 v250, 16, v65
	v_and_b32_e32 v251, 0xffff0000, v65
	s_mov_b32 s38, 0
; DI void add_slots(const Args& A, int tok, int lane, f32x4 (&v)[4]) {
;     ...
; #pragma unroll
;         for (int q = 0; q < 4; ++q) if (ok[q]) {
; #pragma unroll
;             for (int j = 0; j < 4; ++j) { v[j][0] += __uint_as_float(w[q][j].x << 16); v[j][1] += __uint_as_float(w[q][j].x & 0xffff0000u); v[j][2] += __uint_as_float(w[q][j].y << 16); v[j][3] += __uint_as_float(w[q][j].y & 0xffff0000u); } }
.Lrw1_nounp0:
	s_bitcmp1_b32 s33, 0
	s_cbranch_scc0 .Lrw1_a0_0
	v_lshlrev_b32_e32 v128, 16, v98
	v_and_b32_e32 v129, 0xffff0000, v98
	v_lshlrev_b32_e32 v132, 16, v99
	v_and_b32_e32 v133, 0xffff0000, v99
	v_pk_add_f32 v[172:173], v[172:173], v[128:129]
	v_pk_add_f32 v[174:175], v[174:175], v[132:133]
	v_lshlrev_b32_e32 v136, 16, v100
	v_and_b32_e32 v137, 0xffff0000, v100
	v_lshlrev_b32_e32 v252, 16, v101
	v_and_b32_e32 v253, 0xffff0000, v101
	v_pk_add_f32 v[176:177], v[176:177], v[136:137]
	v_pk_add_f32 v[178:179], v[178:179], v[252:253]
	v_lshlrev_b32_e32 v254, 16, v102
	v_and_b32_e32 v255, 0xffff0000, v102
	v_lshlrev_b32_e32 v128, 16, v103
	v_and_b32_e32 v129, 0xffff0000, v103
	v_pk_add_f32 v[180:181], v[180:181], v[254:255]
	v_pk_add_f32 v[182:183], v[182:183], v[128:129]
	v_lshlrev_b32_e32 v132, 16, v104
	v_and_b32_e32 v133, 0xffff0000, v104
	v_lshlrev_b32_e32 v136, 16, v105
	v_and_b32_e32 v137, 0xffff0000, v105
	v_pk_add_f32 v[184:185], v[184:185], v[132:133]
	v_pk_add_f32 v[186:187], v[186:187], v[136:137]
.Lrw1_a0_0:
	s_bitcmp1_b32 s33, 1
	s_cbranch_scc0 .Lrw1_a0_1
	v_lshlrev_b32_e32 v252, 16, v106
	v_and_b32_e32 v253, 0xffff0000, v106
	v_lshlrev_b32_e32 v254, 16, v107
	v_and_b32_e32 v255, 0xffff0000, v107
	v_pk_add_f32 v[172:173], v[172:173], v[252:253]
	v_pk_add_f32 v[174:175], v[174:175], v[254:255]
	v_lshlrev_b32_e32 v128, 16, v108
	v_and_b32_e32 v129, 0xffff0000, v108
	v_lshlrev_b32_e32 v132, 16, v109
	v_and_b32_e32 v133, 0xffff0000, v109
	v_pk_add_f32 v[176:177], v[176:177], v[128:129]
	v_pk_add_f32 v[178:179], v[178:179], v[132:133]
	v_lshlrev_b32_e32 v136, 16, v110
	v_and_b32_e32 v137, 0xffff0000, v110
	v_lshlrev_b32_e32 v252, 16, v111
	v_and_b32_e32 v253, 0xffff0000, v111
	v_pk_add_f32 v[180:181], v[180:181], v[136:137]
	v_pk_add_f32 v[182:183], v[182:183], v[252:253]
	v_lshlrev_b32_e32 v254, 16, v112
	v_and_b32_e32 v255, 0xffff0000, v112
	v_lshlrev_b32_e32 v128, 16, v113
	v_and_b32_e32 v129, 0xffff0000, v113
	v_pk_add_f32 v[184:185], v[184:185], v[254:255]
	v_pk_add_f32 v[186:187], v[186:187], v[128:129]
.Lrw1_a0_1:
	s_bitcmp1_b32 s33, 2
	s_cbranch_scc0 .Lrw1_a0_2
	v_lshlrev_b32_e32 v132, 16, v114
	v_and_b32_e32 v133, 0xffff0000, v114
	v_lshlrev_b32_e32 v136, 16, v115
	v_and_b32_e32 v137, 0xffff0000, v115
	v_pk_add_f32 v[188:189], v[188:189], v[132:133]
	v_pk_add_f32 v[190:191], v[190:191], v[136:137]
	v_lshlrev_b32_e32 v252, 16, v116
	v_and_b32_e32 v253, 0xffff0000, v116
	v_lshlrev_b32_e32 v254, 16, v117
	v_and_b32_e32 v255, 0xffff0000, v117
	v_pk_add_f32 v[192:193], v[192:193], v[252:253]
	v_pk_add_f32 v[194:195], v[194:195], v[254:255]
	v_lshlrev_b32_e32 v128, 16, v118
	v_and_b32_e32 v129, 0xffff0000, v118
	v_lshlrev_b32_e32 v132, 16, v119
	v_and_b32_e32 v133, 0xffff0000, v119
	v_pk_add_f32 v[196:197], v[196:197], v[128:129]
	v_pk_add_f32 v[198:199], v[198:199], v[132:133]
	v_lshlrev_b32_e32 v136, 16, v148
	v_and_b32_e32 v137, 0xffff0000, v148
	v_lshlrev_b32_e32 v252, 16, v149
	v_and_b32_e32 v253, 0xffff0000, v149
	v_pk_add_f32 v[200:201], v[200:201], v[136:137]
	v_pk_add_f32 v[202:203], v[202:203], v[252:253]
.Lrw1_a0_2:
	s_bitcmp1_b32 s33, 3
	s_cbranch_scc0 .Lrw1_a0_3
	v_lshlrev_b32_e32 v254, 16, v150
	v_and_b32_e32 v255, 0xffff0000, v150
	v_lshlrev_b32_e32 v128, 16, v151
	v_and_b32_e32 v129, 0xffff0000, v151
	v_pk_add_f32 v[188:189], v[188:189], v[254:255]
	v_pk_add_f32 v[190:191], v[190:191], v[128:129]
	v_lshlrev_b32_e32 v132, 16, v152
	v_and_b32_e32 v133, 0xffff0000, v152
	v_lshlrev_b32_e32 v136, 16, v153
	v_and_b32_e32 v137, 0xffff0000, v153
	v_pk_add_f32 v[192:193], v[192:193], v[132:133]
	v_pk_add_f32 v[194:195], v[194:195], v[136:137]
	v_lshlrev_b32_e32 v252, 16, v154
	v_and_b32_e32 v253, 0xffff0000, v154
	v_lshlrev_b32_e32 v254, 16, v155
	v_and_b32_e32 v255, 0xffff0000, v155
	v_pk_add_f32 v[196:197], v[196:197], v[252:253]
	v_pk_add_f32 v[198:199], v[198:199], v[254:255]
	v_lshlrev_b32_e32 v128, 16, v156
	v_and_b32_e32 v129, 0xffff0000, v156
	v_lshlrev_b32_e32 v132, 16, v157
	v_and_b32_e32 v133, 0xffff0000, v157
	v_pk_add_f32 v[200:201], v[200:201], v[128:129]
	v_pk_add_f32 v[202:203], v[202:203], v[132:133]
.Lrw1_a0_3:
	s_bitcmp1_b32 s33, 4
	s_cbranch_scc0 .Lrw1_a0_4
	v_lshlrev_b32_e32 v136, 16, v158
	v_and_b32_e32 v137, 0xffff0000, v158
	v_lshlrev_b32_e32 v252, 16, v159
	v_and_b32_e32 v253, 0xffff0000, v159
	v_pk_add_f32 v[204:205], v[204:205], v[136:137]
	v_pk_add_f32 v[206:207], v[206:207], v[252:253]
	v_lshlrev_b32_e32 v254, 16, v160
	v_and_b32_e32 v255, 0xffff0000, v160
	v_lshlrev_b32_e32 v128, 16, v161
	v_and_b32_e32 v129, 0xffff0000, v161
	v_pk_add_f32 v[208:209], v[208:209], v[254:255]
	v_pk_add_f32 v[210:211], v[210:211], v[128:129]
	v_lshlrev_b32_e32 v132, 16, v162
	v_and_b32_e32 v133, 0xffff0000, v162
	v_lshlrev_b32_e32 v136, 16, v163
	v_and_b32_e32 v137, 0xffff0000, v163
	v_pk_add_f32 v[212:213], v[212:213], v[132:133]
	v_pk_add_f32 v[214:215], v[214:215], v[136:137]
	v_lshlrev_b32_e32 v252, 16, v164
	v_and_b32_e32 v253, 0xffff0000, v164
	v_lshlrev_b32_e32 v254, 16, v165
	v_and_b32_e32 v255, 0xffff0000, v165
	v_pk_add_f32 v[216:217], v[216:217], v[252:253]
	v_pk_add_f32 v[218:219], v[218:219], v[254:255]
; DI float wave_sum(float v) { v = row16_sum(v); v += __shfl_xor(v, 16); v += __shfl_xor(v, 32); return v; }
; DI unsigned pkbf(float lo, float hi) { typedef __bf16 b2 __attribute__((ext_vector_type(2))); typedef float f2 __attribute__((ext_vector_type(2))); const f2 v = {lo, hi}; return __builtin_bit_cast(unsigned, __builtin_convertvector(v, b2)); }
; DI void add_slots(const Args& A, int tok, int lane, f32x4 (&v)[4]) {
;     ...
;         for (int q = 0; q < 4; ++q) if (ok[q]) {
; #pragma unroll
;             for (int j = 0; j < 4; ++j) { v[j][0] += __uint_as_float(w[q][j].x << 16); v[j][1] += __uint_as_float(w[q][j].x & 0xffff0000u); v[j][2] += __uint_as_float(w[q][j].y << 16); v[j][3] += __uint_as_float(w[q][j].y & 0xffff0000u); } }
;     }
; }
; DI float row_rstd(const f32x4 (&v)[4]) {
;     float s = 0.f;
; #pragma unroll
;     for (int j = 0; j < 4; ++j) s += (v[j][0] * v[j][0] + v[j][1] * v[j][1]) + (v[j][2] * v[j][2] + v[j][3] * v[j][3]);
;     return rsqrtf(wave_sum(s) * (1.f / DM) + RMS_EPS);
; }
; DI void phase_ln1(const Args& A, int l, int gw, int ngw, int lane) {
;     const float* xin = A.in[I_X]; const bf16* x1 = (const bf16*)(A.ws + WS_X1); bf16* x2 = (bf16*)(A.ws + WS_X2); bf16* hb = (bf16*)(A.ws + WS_HB);
;     f32x4 gg[4];
; #pragma unroll
;     for (int j = 0; j < 4; ++j) gg[j] = ((const f32x4*)(A.in[I_LN1G] + (size_t)l * DM) + lane)[64 * j];
;     for (int tok = gw; tok < NT; tok += 2 * ngw) {
;         const int tokb = tok + ngw; const bool hb2 = tokb < NT;
;         f32x4 va[4], vb[4];
;         if (l == 0) { load_row(xin + (size_t)tok * DM, lane, va); load_row(xin + (size_t)(hb2 ? tokb : tok) * DM, lane, vb); }
;         else { load_row_bf(x1 + (size_t)tok * DM, lane, va); load_row_bf(x1 + (size_t)(hb2 ? tokb : tok) * DM, lane, vb);
;             add_slots(A, tok, lane, va); add_slots(A, hb2 ? tokb : tok, lane, vb);
;             uint2* oa = (uint2*)(x2 + (size_t)tok * DM) + lane; uint2* ob = (uint2*)(x2 + (size_t)tokb * DM) + lane;
; #pragma unroll
;             for (int j = 0; j < 4; ++j) { uint2 w; w.x = pkbf(va[j][0], va[j][1]); w.y = pkbf(va[j][2], va[j][3]); oa[64 * j] = w;
;                 if (hb2) { uint2 u; u.x = pkbf(vb[j][0], vb[j][1]); u.y = pkbf(vb[j][2], vb[j][3]); ob[64 * j] = u; } } }
.Lrw1_a0_4:
	s_bitcmp1_b32 s33, 5
	s_cbranch_scc0 .Lrw1_a0_5
	v_lshlrev_b32_e32 v128, 16, v166
	v_and_b32_e32 v129, 0xffff0000, v166
	v_lshlrev_b32_e32 v132, 16, v167
	v_and_b32_e32 v133, 0xffff0000, v167
	v_pk_add_f32 v[204:205], v[204:205], v[128:129]
	v_pk_add_f32 v[206:207], v[206:207], v[132:133]
	v_lshlrev_b32_e32 v136, 16, v168
	v_and_b32_e32 v137, 0xffff0000, v168
	v_lshlrev_b32_e32 v252, 16, v169
	v_and_b32_e32 v253, 0xffff0000, v169
	v_pk_add_f32 v[208:209], v[208:209], v[136:137]
	v_pk_add_f32 v[210:211], v[210:211], v[252:253]
	v_lshlrev_b32_e32 v254, 16, v220
	v_and_b32_e32 v255, 0xffff0000, v220
	v_lshlrev_b32_e32 v128, 16, v221
	v_and_b32_e32 v129, 0xffff0000, v221
	v_pk_add_f32 v[212:213], v[212:213], v[254:255]
	v_pk_add_f32 v[214:215], v[214:215], v[128:129]
	v_lshlrev_b32_e32 v132, 16, v222
	v_and_b32_e32 v133, 0xffff0000, v222
	v_lshlrev_b32_e32 v136, 16, v223
	v_and_b32_e32 v137, 0xffff0000, v223
	v_pk_add_f32 v[216:217], v[216:217], v[132:133]
	v_pk_add_f32 v[218:219], v[218:219], v[136:137]
.Lrw1_a0_5:
	s_bitcmp1_b32 s33, 6
	s_cbranch_scc0 .Lrw1_a0_6
	v_lshlrev_b32_e32 v252, 16, v224
	v_and_b32_e32 v253, 0xffff0000, v224
	v_lshlrev_b32_e32 v254, 16, v225
	v_and_b32_e32 v255, 0xffff0000, v225
	v_pk_add_f32 v[236:237], v[236:237], v[252:253]
	v_pk_add_f32 v[238:239], v[238:239], v[254:255]
	v_lshlrev_b32_e32 v128, 16, v226
	v_and_b32_e32 v129, 0xffff0000, v226
	v_lshlrev_b32_e32 v132, 16, v227
	v_and_b32_e32 v133, 0xffff0000, v227
	v_pk_add_f32 v[240:241], v[240:241], v[128:129]
	v_pk_add_f32 v[242:243], v[242:243], v[132:133]
	v_lshlrev_b32_e32 v136, 16, v228
	v_and_b32_e32 v137, 0xffff0000, v228
	v_lshlrev_b32_e32 v252, 16, v229
	v_and_b32_e32 v253, 0xffff0000, v229
	v_pk_add_f32 v[244:245], v[244:245], v[136:137]
	v_pk_add_f32 v[246:247], v[246:247], v[252:253]
	v_lshlrev_b32_e32 v254, 16, v230
	v_and_b32_e32 v255, 0xffff0000, v230
	v_lshlrev_b32_e32 v128, 16, v231
	v_and_b32_e32 v129, 0xffff0000, v231
	v_pk_add_f32 v[248:249], v[248:249], v[254:255]
	v_pk_add_f32 v[250:251], v[250:251], v[128:129]
.Lrw1_a0_6:
	s_bitcmp1_b32 s33, 7
	s_cbranch_scc0 .Lrw1_a0_7
	v_lshlrev_b32_e32 v132, 16, v232
	v_and_b32_e32 v133, 0xffff0000, v232
	v_lshlrev_b32_e32 v136, 16, v233
	v_and_b32_e32 v137, 0xffff0000, v233
	v_pk_add_f32 v[236:237], v[236:237], v[132:133]
	v_pk_add_f32 v[238:239], v[238:239], v[136:137]
	v_lshlrev_b32_e32 v252, 16, v140
	v_and_b32_e32 v253, 0xffff0000, v140
	v_lshlrev_b32_e32 v254, 16, v141
	v_and_b32_e32 v255, 0xffff0000, v141
	v_pk_add_f32 v[240:241], v[240:241], v[252:253]
	v_pk_add_f32 v[242:243], v[242:243], v[254:255]
	v_lshlrev_b32_e32 v128, 16, v142
	v_and_b32_e32 v129, 0xffff0000, v142
	v_lshlrev_b32_e32 v132, 16, v143
	v_and_b32_e32 v133, 0xffff0000, v143
	v_pk_add_f32 v[244:245], v[244:245], v[128:129]
	v_pk_add_f32 v[246:247], v[246:247], v[132:133]
	v_lshlrev_b32_e32 v136, 16, v144
	v_and_b32_e32 v137, 0xffff0000, v144
	v_lshlrev_b32_e32 v252, 16, v145
	v_and_b32_e32 v253, 0xffff0000, v145
	v_pk_add_f32 v[248:249], v[248:249], v[136:137]
	v_pk_add_f32 v[250:251], v[250:251], v[252:253]
.Lrw1_a0_7:
	s_or_b32 s34, s66, s68
	s_or_b32 s34, s34, s70
	s_or_b32 s34, s34, s72
	s_cmp_lg_u32 s34, 0
	s_cbranch_scc1 .Lrw1_round0
	v_cvt_pk_bf16_f32 v34, v172, v173
	v_cvt_pk_bf16_f32 v35, v174, v175
	v_cvt_pk_bf16_f32 v36, v176, v177
	v_cvt_pk_bf16_f32 v37, v178, v179
	v_cvt_pk_bf16_f32 v38, v180, v181
	v_cvt_pk_bf16_f32 v39, v182, v183
	v_cvt_pk_bf16_f32 v40, v184, v185
	v_cvt_pk_bf16_f32 v41, v186, v187
	s_mov_b64 s[34:35], s[14:15]
	global_store_dwordx2 v1, v[34:35], s[34:35]
	global_store_dwordx2 v1, v[36:37], s[34:35] offset:512
	global_store_dwordx2 v1, v[38:39], s[34:35] offset:1024
	global_store_dwordx2 v1, v[40:41], s[34:35] offset:1536
	v_cvt_pk_bf16_f32 v42, v188, v189
	v_cvt_pk_bf16_f32 v43, v190, v191
	v_cvt_pk_bf16_f32 v44, v192, v193
	v_cvt_pk_bf16_f32 v45, v194, v195
	v_cvt_pk_bf16_f32 v46, v196, v197
	v_cvt_pk_bf16_f32 v47, v198, v199
	v_cvt_pk_bf16_f32 v48, v200, v201
	v_cvt_pk_bf16_f32 v49, v202, v203
	s_add_u32 s34, s14, 0x400000
	s_addc_u32 s35, s15, 0
	global_store_dwordx2 v1, v[42:43], s[34:35]
	global_store_dwordx2 v1, v[44:45], s[34:35] offset:512
	global_store_dwordx2 v1, v[46:47], s[34:35] offset:1024
	global_store_dwordx2 v1, v[48:49], s[34:35] offset:1536
	v_cvt_pk_bf16_f32 v50, v204, v205
	v_cvt_pk_bf16_f32 v51, v206, v207
	v_cvt_pk_bf16_f32 v52, v208, v209
	v_cvt_pk_bf16_f32 v53, v210, v211
	v_cvt_pk_bf16_f32 v54, v212, v213
	v_cvt_pk_bf16_f32 v55, v214, v215
	v_cvt_pk_bf16_f32 v56, v216, v217
	v_cvt_pk_bf16_f32 v57, v218, v219
	s_add_u32 s34, s14, 0x800000
	s_addc_u32 s35, s15, 0
	global_store_dwordx2 v1, v[50:51], s[34:35]
	global_store_dwordx2 v1, v[52:53], s[34:35] offset:512
	global_store_dwordx2 v1, v[54:55], s[34:35] offset:1024
	global_store_dwordx2 v1, v[56:57], s[34:35] offset:1536
	v_cvt_pk_bf16_f32 v58, v236, v237
	v_cvt_pk_bf16_f32 v59, v238, v239
	v_cvt_pk_bf16_f32 v60, v240, v241
	v_cvt_pk_bf16_f32 v61, v242, v243
	v_cvt_pk_bf16_f32 v62, v244, v245
	v_cvt_pk_bf16_f32 v63, v246, v247
	v_cvt_pk_bf16_f32 v64, v248, v249
	v_cvt_pk_bf16_f32 v65, v250, v251
	s_add_u32 s34, s14, 0xc00000
	s_addc_u32 s35, s15, 0
	global_store_dwordx2 v1, v[58:59], s[34:35]
	global_store_dwordx2 v1, v[60:61], s[34:35] offset:512
	global_store_dwordx2 v1, v[62:63], s[34:35] offset:1024
	global_store_dwordx2 v1, v[64:65], s[34:35] offset:1536
	v_mul_f32_e32 v128, v172, v172
	v_mul_f32_e32 v129, v174, v174
	v_fmac_f32_e32 v128, v173, v173
	v_fmac_f32_e32 v129, v175, v175
	v_add_f32_e32 v128, v128, v129
	v_mul_f32_e32 v132, v188, v188
	v_mul_f32_e32 v133, v190, v190
	v_fmac_f32_e32 v132, v189, v189
; #define DPPF(v, ctrl) __uint_as_float((unsigned)__builtin_amdgcn_update_dpp(0, (int)__float_as_uint(v), (ctrl), 0xf, 0xf, true))
; DI float row16_sum(float v) { v += DPPF(v, 0xB1); v += DPPF(v, 0x4E); v += DPPF(v, 0x141); v += DPPF(v, 0x140); return v; }
; DI float wave_sum(float v) { v = row16_sum(v); v += __shfl_xor(v, 16); v += __shfl_xor(v, 32); return v; }
; DI float row_rstd(const f32x4 (&v)[4]) {
;     float s = 0.f;
; #pragma unroll
;     for (int j = 0; j < 4; ++j) s += (v[j][0] * v[j][0] + v[j][1] * v[j][1]) + (v[j][2] * v[j][2] + v[j][3] * v[j][3]);
;     return rsqrtf(wave_sum(s) * (1.f / DM) + RMS_EPS);
	v_fmac_f32_e32 v133, v191, v191
	v_add_f32_e32 v132, v132, v133
	v_mul_f32_e32 v136, v204, v204
	v_mul_f32_e32 v137, v206, v206
	v_fmac_f32_e32 v136, v205, v205
	v_fmac_f32_e32 v137, v207, v207
	v_add_f32_e32 v136, v136, v137
	v_mul_f32_e32 v252, v236, v236
	v_mul_f32_e32 v253, v238, v238
	v_fmac_f32_e32 v252, v237, v237
	v_fmac_f32_e32 v253, v239, v239
	v_add_f32_e32 v252, v252, v253
	v_mul_f32_e32 v129, v176, v176
	v_mul_f32_e32 v254, v178, v178
	v_fmac_f32_e32 v129, v177, v177
	v_fmac_f32_e32 v254, v179, v179
	v_add_f32_e32 v129, v129, v254
	v_add_f32_e32 v128, v128, v129
	v_mul_f32_e32 v133, v192, v192
	v_mul_f32_e32 v255, v194, v194
	v_fmac_f32_e32 v133, v193, v193
	v_fmac_f32_e32 v255, v195, v195
	v_add_f32_e32 v133, v133, v255
	v_add_f32_e32 v132, v132, v133
	v_mul_f32_e32 v137, v208, v208
	v_mul_f32_e32 v254, v210, v210
	v_fmac_f32_e32 v137, v209, v209
	v_fmac_f32_e32 v254, v211, v211
	v_add_f32_e32 v137, v137, v254
	v_add_f32_e32 v136, v136, v137
	v_mul_f32_e32 v253, v240, v240
	v_mul_f32_e32 v255, v242, v242
	v_fmac_f32_e32 v253, v241, v241
	v_fmac_f32_e32 v255, v243, v243
	v_add_f32_e32 v253, v253, v255
	v_add_f32_e32 v252, v252, v253
	v_mul_f32_e32 v129, v180, v180
	v_mul_f32_e32 v254, v182, v182
	v_fmac_f32_e32 v129, v181, v181
	v_fmac_f32_e32 v254, v183, v183
	v_add_f32_e32 v129, v129, v254
	v_add_f32_e32 v128, v128, v129
	v_mul_f32_e32 v133, v196, v196
	v_mul_f32_e32 v255, v198, v198
	v_fmac_f32_e32 v133, v197, v197
	v_fmac_f32_e32 v255, v199, v199
	v_add_f32_e32 v133, v133, v255
	v_add_f32_e32 v132, v132, v133
	v_mul_f32_e32 v137, v212, v212
	v_mul_f32_e32 v254, v214, v214
	v_fmac_f32_e32 v137, v213, v213
	v_fmac_f32_e32 v254, v215, v215
	v_add_f32_e32 v137, v137, v254
	v_add_f32_e32 v136, v136, v137
	v_mul_f32_e32 v253, v244, v244
	v_mul_f32_e32 v255, v246, v246
	v_fmac_f32_e32 v253, v245, v245
	v_fmac_f32_e32 v255, v247, v247
	v_add_f32_e32 v253, v253, v255
	v_add_f32_e32 v252, v252, v253
	v_mul_f32_e32 v129, v184, v184
	v_mul_f32_e32 v254, v186, v186
	v_fmac_f32_e32 v129, v185, v185
	v_fmac_f32_e32 v254, v187, v187
	v_add_f32_e32 v129, v129, v254
	v_add_f32_e32 v128, v128, v129
	v_mul_f32_e32 v133, v200, v200
	v_mul_f32_e32 v255, v202, v202
	v_fmac_f32_e32 v133, v201, v201
	v_fmac_f32_e32 v255, v203, v203
	v_add_f32_e32 v133, v133, v255
	v_add_f32_e32 v132, v132, v133
	v_mul_f32_e32 v137, v216, v216
	v_mul_f32_e32 v254, v218, v218
	v_fmac_f32_e32 v137, v217, v217
	v_fmac_f32_e32 v254, v219, v219
	v_add_f32_e32 v137, v137, v254
	v_add_f32_e32 v136, v136, v137
	v_mul_f32_e32 v253, v248, v248
	v_mul_f32_e32 v255, v250, v250
	v_fmac_f32_e32 v253, v249, v249
	v_fmac_f32_e32 v255, v251, v251
	v_add_f32_e32 v253, v253, v255
	v_add_f32_e32 v252, v252, v253
	s_nop 0
	ds_bpermute_b32 v129, v4, v128
	ds_bpermute_b32 v133, v4, v132
	ds_bpermute_b32 v137, v4, v136
	ds_bpermute_b32 v253, v4, v252
	s_waitcnt lgkmcnt(0)
	v_add_f32_e32 v128, v128, v129
	v_add_f32_e32 v132, v132, v133
	v_add_f32_e32 v136, v136, v137
	v_add_f32_e32 v252, v252, v253
	s_nop 0
	ds_bpermute_b32 v129, v5, v128
	ds_bpermute_b32 v133, v5, v132
	ds_bpermute_b32 v137, v5, v136
	ds_bpermute_b32 v253, v5, v252
	s_waitcnt lgkmcnt(0)
	v_add_f32_e32 v128, v128, v129
	v_add_f32_e32 v132, v132, v133
	v_add_f32_e32 v136, v136, v137
	v_add_f32_e32 v252, v252, v253
	s_nop 0
	ds_bpermute_b32 v129, v6, v128
	ds_bpermute_b32 v133, v6, v132
	ds_bpermute_b32 v137, v6, v136
	ds_bpermute_b32 v253, v6, v252
	s_waitcnt lgkmcnt(0)
	v_add_f32_e32 v128, v128, v129
	v_add_f32_e32 v132, v132, v133
	v_add_f32_e32 v136, v136, v137
	v_add_f32_e32 v252, v252, v253
	s_nop 0
	ds_bpermute_b32 v129, v7, v128
	ds_bpermute_b32 v133, v7, v132
	ds_bpermute_b32 v137, v7, v136
	ds_bpermute_b32 v253, v7, v252
	s_waitcnt lgkmcnt(0)
	v_add_f32_e32 v128, v128, v129
	v_add_f32_e32 v132, v132, v133
	v_add_f32_e32 v136, v136, v137
	v_add_f32_e32 v252, v252, v253
	s_nop 0
	ds_bpermute_b32 v129, v8, v128
	ds_bpermute_b32 v133, v8, v132
	ds_bpermute_b32 v137, v8, v136
	ds_bpermute_b32 v253, v8, v252
	s_waitcnt lgkmcnt(0)
	v_add_f32_e32 v128, v128, v129
	v_add_f32_e32 v132, v132, v133
	v_add_f32_e32 v136, v136, v137
	v_add_f32_e32 v252, v252, v253
	s_nop 0
	ds_bpermute_b32 v129, v9, v128
	ds_bpermute_b32 v133, v9, v132
	ds_bpermute_b32 v137, v9, v136
	ds_bpermute_b32 v253, v9, v252
	s_waitcnt lgkmcnt(0)
; DI float wave_sum(float v) { v = row16_sum(v); v += __shfl_xor(v, 16); v += __shfl_xor(v, 32); return v; }
; DI unsigned pkbf(float lo, float hi) { typedef __bf16 b2 __attribute__((ext_vector_type(2))); typedef float f2 __attribute__((ext_vector_type(2))); const f2 v = {lo, hi}; return __builtin_bit_cast(unsigned, __builtin_convertvector(v, b2)); }
; DI float row_rstd(const f32x4 (&v)[4]) {
;     ...
;     return rsqrtf(wave_sum(s) * (1.f / DM) + RMS_EPS);
; DI void phase_ln1(const Args& A, int l, int gw, int ngw, int lane) {
;     ...
;         const float ra = row_rstd(va), rb = row_rstd(vb); uint2* o8a = (uint2*)(hb + (size_t)tok * DM) + lane; uint2* o8b = (uint2*)(hb + (size_t)tokb * DM) + lane;
; #pragma unroll
;         for (int j = 0; j < 4; ++j) { uint2 w; w.x = pkbf(va[j][0] * ra * gg[j][0], va[j][1] * ra * gg[j][1]); w.y = pkbf(va[j][2] * ra * gg[j][2], va[j][3] * ra * gg[j][3]); o8a[64 * j] = w;
;             if (hb2) { uint2 u; u.x = pkbf(vb[j][0] * rb * gg[j][0], vb[j][1] * rb * gg[j][1]); u.y = pkbf(vb[j][2] * rb * gg[j][2], vb[j][3] * rb * gg[j][3]); o8b[64 * j] = u; } }
	v_add_f32_e32 v128, v128, v129
	v_add_f32_e32 v132, v132, v133
	v_add_f32_e32 v136, v136, v137
	v_add_f32_e32 v252, v252, v253
	v_fma_f32 v128, v128, s39, v171
	v_mul_f32_e32 v129, 0x4b800000, v128
	v_cmp_gt_f32_e32 vcc, s40, v128
	s_nop 1
	v_cndmask_b32_e32 v128, v128, v129, vcc
	v_rsq_f32_e32 v128, v128
	s_nop 0
	v_mul_f32_e32 v129, 0x45800000, v128
	v_cndmask_b32_e32 v128, v128, v129, vcc
	v_fma_f32 v132, v132, s39, v171
	v_mul_f32_e32 v133, 0x4b800000, v132
	v_cmp_gt_f32_e32 vcc, s40, v132
	s_nop 1
	v_cndmask_b32_e32 v132, v132, v133, vcc
	v_rsq_f32_e32 v132, v132
	s_nop 0
	v_mul_f32_e32 v133, 0x45800000, v132
	v_cndmask_b32_e32 v132, v132, v133, vcc
	v_fma_f32 v136, v136, s39, v171
	v_mul_f32_e32 v137, 0x4b800000, v136
	v_cmp_gt_f32_e32 vcc, s40, v136
	s_nop 1
	v_cndmask_b32_e32 v136, v136, v137, vcc
	v_rsq_f32_e32 v136, v136
	s_nop 0
	v_mul_f32_e32 v137, 0x45800000, v136
	v_cndmask_b32_e32 v136, v136, v137, vcc
	v_fma_f32 v252, v252, s39, v171
	v_mul_f32_e32 v253, 0x4b800000, v252
	v_cmp_gt_f32_e32 vcc, s40, v252
	s_nop 1
	v_cndmask_b32_e32 v252, v252, v253, vcc
	v_rsq_f32_e32 v252, v252
	s_nop 0
	v_mul_f32_e32 v253, 0x45800000, v252
	v_cndmask_b32_e32 v252, v252, v253, vcc
	v_pk_mul_f32 v[172:173], v[172:173], v[128:129] op_sel_hi:[1,0]
	v_pk_mul_f32 v[174:175], v[174:175], v[128:129] op_sel_hi:[1,0]
	v_pk_mul_f32 v[176:177], v[176:177], v[128:129] op_sel_hi:[1,0]
	v_pk_mul_f32 v[178:179], v[178:179], v[128:129] op_sel_hi:[1,0]
	v_pk_mul_f32 v[180:181], v[180:181], v[128:129] op_sel_hi:[1,0]
	v_pk_mul_f32 v[182:183], v[182:183], v[128:129] op_sel_hi:[1,0]
	v_pk_mul_f32 v[184:185], v[184:185], v[128:129] op_sel_hi:[1,0]
	v_pk_mul_f32 v[186:187], v[186:187], v[128:129] op_sel_hi:[1,0]
	v_pk_mul_f32 v[172:173], v[172:173], v[18:19]
	v_pk_mul_f32 v[174:175], v[174:175], v[20:21]
	v_pk_mul_f32 v[176:177], v[176:177], v[22:23]
	v_pk_mul_f32 v[178:179], v[178:179], v[24:25]
	v_pk_mul_f32 v[180:181], v[180:181], v[26:27]
	v_pk_mul_f32 v[182:183], v[182:183], v[28:29]
	v_pk_mul_f32 v[184:185], v[184:185], v[30:31]
	v_pk_mul_f32 v[186:187], v[186:187], v[32:33]
	v_cvt_pk_bf16_f32 v34, v172, v173
	v_cvt_pk_bf16_f32 v35, v174, v175
	v_cvt_pk_bf16_f32 v36, v176, v177
	v_cvt_pk_bf16_f32 v37, v178, v179
	v_cvt_pk_bf16_f32 v38, v180, v181
	v_cvt_pk_bf16_f32 v39, v182, v183
	v_cvt_pk_bf16_f32 v40, v184, v185
	v_cvt_pk_bf16_f32 v41, v186, v187
	s_mov_b64 s[34:35], s[16:17]
	global_store_dwordx2 v1, v[34:35], s[34:35]
	global_store_dwordx2 v1, v[36:37], s[34:35] offset:512
	global_store_dwordx2 v1, v[38:39], s[34:35] offset:1024
	global_store_dwordx2 v1, v[40:41], s[34:35] offset:1536
	v_pk_mul_f32 v[188:189], v[188:189], v[132:133] op_sel_hi:[1,0]
	v_pk_mul_f32 v[190:191], v[190:191], v[132:133] op_sel_hi:[1,0]
	v_pk_mul_f32 v[192:193], v[192:193], v[132:133] op_sel_hi:[1,0]
	v_pk_mul_f32 v[194:195], v[194:195], v[132:133] op_sel_hi:[1,0]
	v_pk_mul_f32 v[196:197], v[196:197], v[132:133] op_sel_hi:[1,0]
	v_pk_mul_f32 v[198:199], v[198:199], v[132:133] op_sel_hi:[1,0]
	v_pk_mul_f32 v[200:201], v[200:201], v[132:133] op_sel_hi:[1,0]
	v_pk_mul_f32 v[202:203], v[202:203], v[132:133] op_sel_hi:[1,0]
	v_pk_mul_f32 v[188:189], v[188:189], v[18:19]
	v_pk_mul_f32 v[190:191], v[190:191], v[20:21]
	v_pk_mul_f32 v[192:193], v[192:193], v[22:23]
	v_pk_mul_f32 v[194:195], v[194:195], v[24:25]
	v_pk_mul_f32 v[196:197], v[196:197], v[26:27]
	v_pk_mul_f32 v[198:199], v[198:199], v[28:29]
	v_pk_mul_f32 v[200:201], v[200:201], v[30:31]
	v_pk_mul_f32 v[202:203], v[202:203], v[32:33]
	v_cvt_pk_bf16_f32 v42, v188, v189
	v_cvt_pk_bf16_f32 v43, v190, v191
	v_cvt_pk_bf16_f32 v44, v192, v193
	v_cvt_pk_bf16_f32 v45, v194, v195
	v_cvt_pk_bf16_f32 v46, v196, v197
	v_cvt_pk_bf16_f32 v47, v198, v199
	v_cvt_pk_bf16_f32 v48, v200, v201
	v_cvt_pk_bf16_f32 v49, v202, v203
	s_add_u32 s34, s16, 0x400000
	s_addc_u32 s35, s17, 0
	global_store_dwordx2 v1, v[42:43], s[34:35]
	global_store_dwordx2 v1, v[44:45], s[34:35] offset:512
	global_store_dwordx2 v1, v[46:47], s[34:35] offset:1024
	global_store_dwordx2 v1, v[48:49], s[34:35] offset:1536
	v_pk_mul_f32 v[204:205], v[204:205], v[136:137] op_sel_hi:[1,0]
	v_pk_mul_f32 v[206:207], v[206:207], v[136:137] op_sel_hi:[1,0]
	v_pk_mul_f32 v[208:209], v[208:209], v[136:137] op_sel_hi:[1,0]
	v_pk_mul_f32 v[210:211], v[210:211], v[136:137] op_sel_hi:[1,0]
	v_pk_mul_f32 v[212:213], v[212:213], v[136:137] op_sel_hi:[1,0]
	v_pk_mul_f32 v[214:215], v[214:215], v[136:137] op_sel_hi:[1,0]
	v_pk_mul_f32 v[216:217], v[216:217], v[136:137] op_sel_hi:[1,0]
	v_pk_mul_f32 v[218:219], v[218:219], v[136:137] op_sel_hi:[1,0]
	v_pk_mul_f32 v[204:205], v[204:205], v[18:19]
	v_pk_mul_f32 v[206:207], v[206:207], v[20:21]
	v_pk_mul_f32 v[208:209], v[208:209], v[22:23]
	v_pk_mul_f32 v[210:211], v[210:211], v[24:25]
	v_pk_mul_f32 v[212:213], v[212:213], v[26:27]
	v_pk_mul_f32 v[214:215], v[214:215], v[28:29]
	v_pk_mul_f32 v[216:217], v[216:217], v[30:31]
	v_pk_mul_f32 v[218:219], v[218:219], v[32:33]
	v_cvt_pk_bf16_f32 v50, v204, v205
	v_cvt_pk_bf16_f32 v51, v206, v207
	v_cvt_pk_bf16_f32 v52, v208, v209
	v_cvt_pk_bf16_f32 v53, v210, v211
	v_cvt_pk_bf16_f32 v54, v212, v213
	v_cvt_pk_bf16_f32 v55, v214, v215
	v_cvt_pk_bf16_f32 v56, v216, v217
	v_cvt_pk_bf16_f32 v57, v218, v219
	s_add_u32 s34, s16, 0x800000
	s_addc_u32 s35, s17, 0
	global_store_dwordx2 v1, v[50:51], s[34:35]
	global_store_dwordx2 v1, v[52:53], s[34:35] offset:512
	global_store_dwordx2 v1, v[54:55], s[34:35] offset:1024
	global_store_dwordx2 v1, v[56:57], s[34:35] offset:1536
	v_pk_mul_f32 v[236:237], v[236:237], v[252:253] op_sel_hi:[1,0]
	v_pk_mul_f32 v[238:239], v[238:239], v[252:253] op_sel_hi:[1,0]
	v_pk_mul_f32 v[240:241], v[240:241], v[252:253] op_sel_hi:[1,0]
	v_pk_mul_f32 v[242:243], v[242:243], v[252:253] op_sel_hi:[1,0]
	v_pk_mul_f32 v[244:245], v[244:245], v[252:253] op_sel_hi:[1,0]
	v_pk_mul_f32 v[246:247], v[246:247], v[252:253] op_sel_hi:[1,0]
	v_pk_mul_f32 v[248:249], v[248:249], v[252:253] op_sel_hi:[1,0]
	v_pk_mul_f32 v[250:251], v[250:251], v[252:253] op_sel_hi:[1,0]
	v_pk_mul_f32 v[236:237], v[236:237], v[18:19]
	v_pk_mul_f32 v[238:239], v[238:239], v[20:21]
	v_pk_mul_f32 v[240:241], v[240:241], v[22:23]
	v_pk_mul_f32 v[242:243], v[242:243], v[24:25]
	v_pk_mul_f32 v[244:245], v[244:245], v[26:27]
	v_pk_mul_f32 v[246:247], v[246:247], v[28:29]
	v_pk_mul_f32 v[248:249], v[248:249], v[30:31]
	v_pk_mul_f32 v[250:251], v[250:251], v[32:33]
	v_cvt_pk_bf16_f32 v58, v236, v237
	v_cvt_pk_bf16_f32 v59, v238, v239
	v_cvt_pk_bf16_f32 v60, v240, v241
	v_cvt_pk_bf16_f32 v61, v242, v243
	v_cvt_pk_bf16_f32 v62, v244, v245
	v_cvt_pk_bf16_f32 v63, v246, v247
	v_cvt_pk_bf16_f32 v64, v248, v249
	v_cvt_pk_bf16_f32 v65, v250, v251
	s_add_u32 s34, s16, 0xc00000
	s_addc_u32 s35, s17, 0
	global_store_dwordx2 v1, v[58:59], s[34:35]
	global_store_dwordx2 v1, v[60:61], s[34:35] offset:512
	global_store_dwordx2 v1, v[62:63], s[34:35] offset:1024
	global_store_dwordx2 v1, v[64:65], s[34:35] offset:1536
	s_mov_b32 s38, 1
; DI void load_row_bf(const bf16* xrow, int lane, f32x4 (&v)[4]) {
;     const uint2* xr = (const uint2*)xrow + lane;
; #pragma unroll
;     for (int j = 0; j < 4; ++j) { const uint2 w = xr[64 * j]; v[j][0] = __uint_as_float(w.x << 16); v[j][1] = __uint_as_float(w.x & 0xffff0000u); v[j][2] = __uint_as_float(w.y << 16); v[j][3] = __uint_as_float(w.y & 0xffff0000u); }
; }
; DI void add_slots(const Args& A, int tok, int lane, f32x4 (&v)[4]) {
;     ...
;     while (m) {
;         const uint2* p[4]; bool ok[4];
; #pragma unroll
;         for (int q = 0; q < 4; ++q) { ok[q] = m != 0u; const int e = ok[q] ? __builtin_ctz(m) : 0; m &= m - 1u; const int r = __shfl(mys, e);
;             p[q] = (const uint2*)(ys + (size_t)((e * NB + b) * CAP + (ok[q] ? r : 0)) * DM) + lane; }
;         uint2 w[4][4];
; #pragma unroll
;         for (int q = 0; q < 4; ++q) if (ok[q]) {
; #pragma unroll
;             for (int j = 0; j < 4; ++j) w[q][j] = p[q][64 * j]; }
.Lrw1_round1:
	s_mov_b32 s33, 0
	s_cmp_eq_u32 s74, 0
	s_cbranch_scc1 .Lrw1_i1_0
	s_ff1_i32_b32 s34, s74
	s_add_i32 s35, s74, -1
	s_and_b32 s74, s74, s35
	s_nop 1
	v_readlane_b32 s35, v14, s34
	s_lshl_b32 s34, s34, 22
	s_lshl_b32 s35, s35, 11
	s_add_u32 s34, s34, s35
	s_add_u32 s34, s34, 0x200000
	s_add_u32 s36, s12, s34
	s_addc_u32 s37, s13, 0
	global_load_dwordx2 v[98:99], v1, s[36:37]
	global_load_dwordx2 v[100:101], v1, s[36:37] offset:512
	global_load_dwordx2 v[102:103], v1, s[36:37] offset:1024
	global_load_dwordx2 v[104:105], v1, s[36:37] offset:1536
	s_bitset1_b32 s33, 0
.Lrw1_i1_0:
	s_cmp_eq_u32 s74, 0
	s_cbranch_scc1 .Lrw1_i1_1
	s_ff1_i32_b32 s34, s74
	s_add_i32 s35, s74, -1
	s_and_b32 s74, s74, s35
	s_nop 1
	v_readlane_b32 s35, v14, s34
	s_lshl_b32 s34, s34, 22
	s_lshl_b32 s35, s35, 11
	s_add_u32 s34, s34, s35
	s_add_u32 s34, s34, 0x200000
	s_add_u32 s36, s12, s34
	s_addc_u32 s37, s13, 0
	global_load_dwordx2 v[106:107], v1, s[36:37]
	global_load_dwordx2 v[108:109], v1, s[36:37] offset:512
	global_load_dwordx2 v[110:111], v1, s[36:37] offset:1024
	global_load_dwordx2 v[112:113], v1, s[36:37] offset:1536
	s_bitset1_b32 s33, 1
.Lrw1_i1_1:
	s_cmp_eq_u32 s76, 0
	s_cbranch_scc1 .Lrw1_i1_2
	s_ff1_i32_b32 s34, s76
	s_add_i32 s35, s76, -1
	s_and_b32 s76, s76, s35
	s_nop 1
	v_readlane_b32 s35, v15, s34
	s_lshl_b32 s34, s34, 22
	s_lshl_b32 s35, s35, 11
	s_add_u32 s34, s34, s35
	s_add_u32 s34, s34, 0x280000
	s_add_u32 s36, s12, s34
	s_addc_u32 s37, s13, 0
	global_load_dwordx2 v[114:115], v1, s[36:37]
	global_load_dwordx2 v[116:117], v1, s[36:37] offset:512
	global_load_dwordx2 v[118:119], v1, s[36:37] offset:1024
	global_load_dwordx2 v[148:149], v1, s[36:37] offset:1536
	s_bitset1_b32 s33, 2
.Lrw1_i1_2:
	s_cmp_eq_u32 s76, 0
	s_cbranch_scc1 .Lrw1_i1_3
	s_ff1_i32_b32 s34, s76
	s_add_i32 s35, s76, -1
	s_and_b32 s76, s76, s35
	s_nop 1
	v_readlane_b32 s35, v15, s34
	s_lshl_b32 s34, s34, 22
	s_lshl_b32 s35, s35, 11
	s_add_u32 s34, s34, s35
	s_add_u32 s34, s34, 0x280000
	s_add_u32 s36, s12, s34
	s_addc_u32 s37, s13, 0
	global_load_dwordx2 v[150:151], v1, s[36:37]
	global_load_dwordx2 v[152:153], v1, s[36:37] offset:512
	global_load_dwordx2 v[154:155], v1, s[36:37] offset:1024
	global_load_dwordx2 v[156:157], v1, s[36:37] offset:1536
	s_bitset1_b32 s33, 3
.Lrw1_i1_3:
	s_cmp_eq_u32 s78, 0
	s_cbranch_scc1 .Lrw1_i1_4
	s_ff1_i32_b32 s34, s78
	s_add_i32 s35, s78, -1
	s_and_b32 s78, s78, s35
	s_nop 1
	v_readlane_b32 s35, v16, s34
	s_lshl_b32 s34, s34, 22
	s_lshl_b32 s35, s35, 11
	s_add_u32 s34, s34, s35
	s_add_u32 s34, s34, 0x300000
	s_add_u32 s36, s12, s34
	s_addc_u32 s37, s13, 0
	global_load_dwordx2 v[158:159], v1, s[36:37]
	global_load_dwordx2 v[160:161], v1, s[36:37] offset:512
	global_load_dwordx2 v[162:163], v1, s[36:37] offset:1024
	global_load_dwordx2 v[164:165], v1, s[36:37] offset:1536
	s_bitset1_b32 s33, 4
.Lrw1_i1_4:
	s_cmp_eq_u32 s78, 0
	s_cbranch_scc1 .Lrw1_i1_5
	s_ff1_i32_b32 s34, s78
	s_add_i32 s35, s78, -1
	s_and_b32 s78, s78, s35
	s_nop 1
	v_readlane_b32 s35, v16, s34
	s_lshl_b32 s34, s34, 22
	s_lshl_b32 s35, s35, 11
	s_add_u32 s34, s34, s35
	s_add_u32 s34, s34, 0x300000
	s_add_u32 s36, s12, s34
	s_addc_u32 s37, s13, 0
	global_load_dwordx2 v[166:167], v1, s[36:37]
	global_load_dwordx2 v[168:169], v1, s[36:37] offset:512
	global_load_dwordx2 v[220:221], v1, s[36:37] offset:1024
	global_load_dwordx2 v[222:223], v1, s[36:37] offset:1536
	s_bitset1_b32 s33, 5
.Lrw1_i1_5:
	s_cmp_eq_u32 s80, 0
	s_cbranch_scc1 .Lrw1_i1_6
	s_ff1_i32_b32 s34, s80
	s_add_i32 s35, s80, -1
	s_and_b32 s80, s80, s35
	s_nop 1
	v_readlane_b32 s35, v17, s34
	s_lshl_b32 s34, s34, 22
	s_lshl_b32 s35, s35, 11
	s_add_u32 s34, s34, s35
	s_add_u32 s34, s34, 0x380000
	s_add_u32 s36, s12, s34
	s_addc_u32 s37, s13, 0
	global_load_dwordx2 v[224:225], v1, s[36:37]
	global_load_dwordx2 v[226:227], v1, s[36:37] offset:512
	global_load_dwordx2 v[228:229], v1, s[36:37] offset:1024
	global_load_dwordx2 v[230:231], v1, s[36:37] offset:1536
	s_bitset1_b32 s33, 6
.Lrw1_i1_6:
	s_cmp_eq_u32 s80, 0
	s_cbranch_scc1 .Lrw1_i1_7
	s_ff1_i32_b32 s34, s80
	s_add_i32 s35, s80, -1
	s_and_b32 s80, s80, s35
	s_nop 1
	v_readlane_b32 s35, v17, s34
	s_lshl_b32 s34, s34, 22
	s_lshl_b32 s35, s35, 11
	s_add_u32 s34, s34, s35
	s_add_u32 s34, s34, 0x380000
	s_add_u32 s36, s12, s34
	s_addc_u32 s37, s13, 0
	global_load_dwordx2 v[232:233], v1, s[36:37]
	global_load_dwordx2 v[140:141], v1, s[36:37] offset:512
	global_load_dwordx2 v[142:143], v1, s[36:37] offset:1024
	global_load_dwordx2 v[144:145], v1, s[36:37] offset:1536
	s_bitset1_b32 s33, 7
.Lrw1_i1_7:
	s_waitcnt vmcnt(0)
	s_cmp_eq_u32 s38, 0
	s_cbranch_scc1 .Lrw1_nounp1
	v_lshlrev_b32_e32 v172, 16, v66
	v_and_b32_e32 v173, 0xffff0000, v66
	v_lshlrev_b32_e32 v174, 16, v67
	v_and_b32_e32 v175, 0xffff0000, v67
	v_lshlrev_b32_e32 v176, 16, v68
	v_and_b32_e32 v177, 0xffff0000, v68
	v_lshlrev_b32_e32 v178, 16, v69
	v_and_b32_e32 v179, 0xffff0000, v69
	v_lshlrev_b32_e32 v180, 16, v70
	v_and_b32_e32 v181, 0xffff0000, v70
	v_lshlrev_b32_e32 v182, 16, v71
	v_and_b32_e32 v183, 0xffff0000, v71
	v_lshlrev_b32_e32 v184, 16, v72
	v_and_b32_e32 v185, 0xffff0000, v72
	v_lshlrev_b32_e32 v186, 16, v73
	v_and_b32_e32 v187, 0xffff0000, v73
	v_lshlrev_b32_e32 v188, 16, v74
	v_and_b32_e32 v189, 0xffff0000, v74
	v_lshlrev_b32_e32 v190, 16, v75
	v_and_b32_e32 v191, 0xffff0000, v75
	v_lshlrev_b32_e32 v192, 16, v76
	v_and_b32_e32 v193, 0xffff0000, v76
	v_lshlrev_b32_e32 v194, 16, v77
	v_and_b32_e32 v195, 0xffff0000, v77
	v_lshlrev_b32_e32 v196, 16, v78
	v_and_b32_e32 v197, 0xffff0000, v78
	v_lshlrev_b32_e32 v198, 16, v79
	v_and_b32_e32 v199, 0xffff0000, v79
	v_lshlrev_b32_e32 v200, 16, v80
	v_and_b32_e32 v201, 0xffff0000, v80
	v_lshlrev_b32_e32 v202, 16, v81
	v_and_b32_e32 v203, 0xffff0000, v81
	v_lshlrev_b32_e32 v204, 16, v82
	v_and_b32_e32 v205, 0xffff0000, v82
	v_lshlrev_b32_e32 v206, 16, v83
	v_and_b32_e32 v207, 0xffff0000, v83
	v_lshlrev_b32_e32 v208, 16, v84
	v_and_b32_e32 v209, 0xffff0000, v84
	v_lshlrev_b32_e32 v210, 16, v85
	v_and_b32_e32 v211, 0xffff0000, v85
	v_lshlrev_b32_e32 v212, 16, v86
	v_and_b32_e32 v213, 0xffff0000, v86
	v_lshlrev_b32_e32 v214, 16, v87
	v_and_b32_e32 v215, 0xffff0000, v87
	v_lshlrev_b32_e32 v216, 16, v88
	v_and_b32_e32 v217, 0xffff0000, v88
	v_lshlrev_b32_e32 v218, 16, v89
	v_and_b32_e32 v219, 0xffff0000, v89
	v_lshlrev_b32_e32 v236, 16, v90
	v_and_b32_e32 v237, 0xffff0000, v90
	v_lshlrev_b32_e32 v238, 16, v91
	v_and_b32_e32 v239, 0xffff0000, v91
	v_lshlrev_b32_e32 v240, 16, v92
	v_and_b32_e32 v241, 0xffff0000, v92
	v_lshlrev_b32_e32 v242, 16, v93
	v_and_b32_e32 v243, 0xffff0000, v93
	v_lshlrev_b32_e32 v244, 16, v94
	v_and_b32_e32 v245, 0xffff0000, v94
	v_lshlrev_b32_e32 v246, 16, v95
	v_and_b32_e32 v247, 0xffff0000, v95
	v_lshlrev_b32_e32 v248, 16, v96
	v_and_b32_e32 v249, 0xffff0000, v96
	v_lshlrev_b32_e32 v250, 16, v97
	v_and_b32_e32 v251, 0xffff0000, v97
	s_mov_b32 s38, 0

; DI float wave_sum(float v) { v = row16_sum(v); v += __shfl_xor(v, 16); v += __shfl_xor(v, 32); return v; }
; DI unsigned pkbf(float lo, float hi) { typedef __bf16 b2 __attribute__((ext_vector_type(2))); typedef float f2 __attribute__((ext_vector_type(2))); const f2 v = {lo, hi}; return __builtin_bit_cast(unsigned, __builtin_convertvector(v, b2)); }
; DI float row_rstd(const f32x4 (&v)[4]) {
;     float s = 0.f;
; #pragma unroll
;     for (int j = 0; j < 4; ++j) s += (v[j][0] * v[j][0] + v[j][1] * v[j][1]) + (v[j][2] * v[j][2] + v[j][3] * v[j][3]);
;     return rsqrtf(wave_sum(s) * (1.f / DM) + RMS_EPS);
; DI void phase_ln1(const Args& A, int l, int gw, int ngw, int lane) {
;     ...
;             uint2* oa = (uint2*)(x2 + (size_t)tok * DM) + lane; uint2* ob = (uint2*)(x2 + (size_t)tokb * DM) + lane;
; #pragma unroll
;             for (int j = 0; j < 4; ++j) { uint2 w; w.x = pkbf(va[j][0], va[j][1]); w.y = pkbf(va[j][2], va[j][3]); oa[64 * j] = w;
;                 if (hb2) { uint2 u; u.x = pkbf(vb[j][0], vb[j][1]); u.y = pkbf(vb[j][2], vb[j][3]); ob[64 * j] = u; } } }
;         const float ra = row_rstd(va), rb = row_rstd(vb); uint2* o8a = (uint2*)(hb + (size_t)tok * DM) + lane; uint2* o8b = (uint2*)(hb + (size_t)tokb * DM) + lane;
; #pragma unroll
;         for (int j = 0; j < 4; ++j) { uint2 w; w.x = pkbf(va[j][0] * ra * gg[j][0], va[j][1] * ra * gg[j][1]); w.y = pkbf(va[j][2] * ra * gg[j][2], va[j][3] * ra * gg[j][3]); o8a[64 * j] = w;
;             if (hb2) { uint2 u; u.x = pkbf(vb[j][0] * rb * gg[j][0], vb[j][1] * rb * gg[j][1]); u.y = pkbf(vb[j][2] * rb * gg[j][2], vb[j][3] * rb * gg[j][3]); o8b[64 * j] = u; } }
.Lrw1_a1_7:
	s_or_b32 s34, s74, s76
	s_or_b32 s34, s34, s78
	s_or_b32 s34, s34, s80
	s_cmp_lg_u32 s34, 0
	s_cbranch_scc1 .Lrw1_round1
	v_cvt_pk_bf16_f32 v66, v172, v173
	v_cvt_pk_bf16_f32 v67, v174, v175
	v_cvt_pk_bf16_f32 v68, v176, v177
	v_cvt_pk_bf16_f32 v69, v178, v179
	v_cvt_pk_bf16_f32 v70, v180, v181
	v_cvt_pk_bf16_f32 v71, v182, v183
	v_cvt_pk_bf16_f32 v72, v184, v185
	v_cvt_pk_bf16_f32 v73, v186, v187
	s_add_u32 s34, s14, 0x1000000
	s_addc_u32 s35, s15, 0
	global_store_dwordx2 v1, v[66:67], s[34:35]
	global_store_dwordx2 v1, v[68:69], s[34:35] offset:512
	global_store_dwordx2 v1, v[70:71], s[34:35] offset:1024
	global_store_dwordx2 v1, v[72:73], s[34:35] offset:1536
	v_cvt_pk_bf16_f32 v74, v188, v189
	v_cvt_pk_bf16_f32 v75, v190, v191
	v_cvt_pk_bf16_f32 v76, v192, v193
	v_cvt_pk_bf16_f32 v77, v194, v195
	v_cvt_pk_bf16_f32 v78, v196, v197
	v_cvt_pk_bf16_f32 v79, v198, v199
	v_cvt_pk_bf16_f32 v80, v200, v201
	v_cvt_pk_bf16_f32 v81, v202, v203
	s_add_u32 s34, s14, 0x1400000
	s_addc_u32 s35, s15, 0
	global_store_dwordx2 v1, v[74:75], s[34:35]
	global_store_dwordx2 v1, v[76:77], s[34:35] offset:512
	global_store_dwordx2 v1, v[78:79], s[34:35] offset:1024
	global_store_dwordx2 v1, v[80:81], s[34:35] offset:1536
	v_cvt_pk_bf16_f32 v82, v204, v205
	v_cvt_pk_bf16_f32 v83, v206, v207
	v_cvt_pk_bf16_f32 v84, v208, v209
	v_cvt_pk_bf16_f32 v85, v210, v211
	v_cvt_pk_bf16_f32 v86, v212, v213
	v_cvt_pk_bf16_f32 v87, v214, v215
	v_cvt_pk_bf16_f32 v88, v216, v217
	v_cvt_pk_bf16_f32 v89, v218, v219
	s_add_u32 s34, s14, 0x1800000
	s_addc_u32 s35, s15, 0
	global_store_dwordx2 v1, v[82:83], s[34:35]
	global_store_dwordx2 v1, v[84:85], s[34:35] offset:512
	global_store_dwordx2 v1, v[86:87], s[34:35] offset:1024
	global_store_dwordx2 v1, v[88:89], s[34:35] offset:1536
	v_cvt_pk_bf16_f32 v90, v236, v237
	v_cvt_pk_bf16_f32 v91, v238, v239
	v_cvt_pk_bf16_f32 v92, v240, v241
	v_cvt_pk_bf16_f32 v93, v242, v243
	v_cvt_pk_bf16_f32 v94, v244, v245
	v_cvt_pk_bf16_f32 v95, v246, v247
	v_cvt_pk_bf16_f32 v96, v248, v249
	v_cvt_pk_bf16_f32 v97, v250, v251
	s_add_u32 s34, s14, 0x1c00000
	s_addc_u32 s35, s15, 0
	global_store_dwordx2 v1, v[90:91], s[34:35]
	global_store_dwordx2 v1, v[92:93], s[34:35] offset:512
	global_store_dwordx2 v1, v[94:95], s[34:35] offset:1024
	global_store_dwordx2 v1, v[96:97], s[34:35] offset:1536
	v_mul_f32_e32 v128, v172, v172
	v_mul_f32_e32 v129, v174, v174
	v_fmac_f32_e32 v128, v173, v173
	v_fmac_f32_e32 v129, v175, v175
	v_add_f32_e32 v128, v128, v129
	v_mul_f32_e32 v132, v188, v188
	v_mul_f32_e32 v133, v190, v190
	v_fmac_f32_e32 v132, v189, v189
	v_fmac_f32_e32 v133, v191, v191
	v_add_f32_e32 v132, v132, v133
	v_mul_f32_e32 v136, v204, v204
	v_mul_f32_e32 v137, v206, v206
	v_fmac_f32_e32 v136, v205, v205
	v_fmac_f32_e32 v137, v207, v207
	v_add_f32_e32 v136, v136, v137
	v_mul_f32_e32 v252, v236, v236
	v_mul_f32_e32 v253, v238, v238
	v_fmac_f32_e32 v252, v237, v237
	v_fmac_f32_e32 v253, v239, v239
	v_add_f32_e32 v252, v252, v253
	v_mul_f32_e32 v129, v176, v176
	v_mul_f32_e32 v254, v178, v178
	v_fmac_f32_e32 v129, v177, v177
	v_fmac_f32_e32 v254, v179, v179
	v_add_f32_e32 v129, v129, v254
	v_add_f32_e32 v128, v128, v129
	v_mul_f32_e32 v133, v192, v192
	v_mul_f32_e32 v255, v194, v194
	v_fmac_f32_e32 v133, v193, v193
	v_fmac_f32_e32 v255, v195, v195
	v_add_f32_e32 v133, v133, v255
	v_add_f32_e32 v132, v132, v133
	v_mul_f32_e32 v137, v208, v208
	v_mul_f32_e32 v254, v210, v210
	v_fmac_f32_e32 v137, v209, v209
	v_fmac_f32_e32 v254, v211, v211
	v_add_f32_e32 v137, v137, v254
	v_add_f32_e32 v136, v136, v137
	v_mul_f32_e32 v253, v240, v240
	v_mul_f32_e32 v255, v242, v242
	v_fmac_f32_e32 v253, v241, v241
	v_fmac_f32_e32 v255, v243, v243
	v_add_f32_e32 v253, v253, v255
	v_add_f32_e32 v252, v252, v253
	v_mul_f32_e32 v129, v180, v180
	v_mul_f32_e32 v254, v182, v182
	v_fmac_f32_e32 v129, v181, v181
	v_fmac_f32_e32 v254, v183, v183
	v_add_f32_e32 v129, v129, v254
	v_add_f32_e32 v128, v128, v129
	v_mul_f32_e32 v133, v196, v196
	v_mul_f32_e32 v255, v198, v198
	v_fmac_f32_e32 v133, v197, v197
	v_fmac_f32_e32 v255, v199, v199
	v_add_f32_e32 v133, v133, v255
	v_add_f32_e32 v132, v132, v133
	v_mul_f32_e32 v137, v212, v212
	v_mul_f32_e32 v254, v214, v214
	v_fmac_f32_e32 v137, v213, v213
	v_fmac_f32_e32 v254, v215, v215
	v_add_f32_e32 v137, v137, v254
	v_add_f32_e32 v136, v136, v137
	v_mul_f32_e32 v253, v244, v244
	v_mul_f32_e32 v255, v246, v246
	v_fmac_f32_e32 v253, v245, v245
	v_fmac_f32_e32 v255, v247, v247
	v_add_f32_e32 v253, v253, v255
	v_add_f32_e32 v252, v252, v253
	v_mul_f32_e32 v129, v184, v184
	v_mul_f32_e32 v254, v186, v186
	v_fmac_f32_e32 v129, v185, v185
	v_fmac_f32_e32 v254, v187, v187
	v_add_f32_e32 v129, v129, v254
	v_add_f32_e32 v128, v128, v129
	v_mul_f32_e32 v133, v200, v200
	v_mul_f32_e32 v255, v202, v202
	v_fmac_f32_e32 v133, v201, v201
	v_fmac_f32_e32 v255, v203, v203
	v_add_f32_e32 v133, v133, v255
	v_add_f32_e32 v132, v132, v133
	v_mul_f32_e32 v137, v216, v216
	v_mul_f32_e32 v254, v218, v218
	v_fmac_f32_e32 v137, v217, v217
	v_fmac_f32_e32 v254, v219, v219
	v_add_f32_e32 v137, v137, v254
	v_add_f32_e32 v136, v136, v137
	v_mul_f32_e32 v253, v248, v248
	v_mul_f32_e32 v255, v250, v250
	v_fmac_f32_e32 v253, v249, v249
	v_fmac_f32_e32 v255, v251, v251
	v_add_f32_e32 v253, v253, v255
	v_add_f32_e32 v252, v252, v253
	s_nop 0
	ds_bpermute_b32 v129, v4, v128
	ds_bpermute_b32 v133, v4, v132
	ds_bpermute_b32 v137, v4, v136
	ds_bpermute_b32 v253, v4, v252
	s_waitcnt lgkmcnt(0)
	v_add_f32_e32 v128, v128, v129
	v_add_f32_e32 v132, v132, v133
	v_add_f32_e32 v136, v136, v137
	v_add_f32_e32 v252, v252, v253
	s_nop 0
	ds_bpermute_b32 v129, v5, v128
	ds_bpermute_b32 v133, v5, v132
	ds_bpermute_b32 v137, v5, v136
	ds_bpermute_b32 v253, v5, v252
	s_waitcnt lgkmcnt(0)
; DI float wave_sum(float v) { v = row16_sum(v); v += __shfl_xor(v, 16); v += __shfl_xor(v, 32); return v; }
; DI unsigned pkbf(float lo, float hi) { typedef __bf16 b2 __attribute__((ext_vector_type(2))); typedef float f2 __attribute__((ext_vector_type(2))); const f2 v = {lo, hi}; return __builtin_bit_cast(unsigned, __builtin_convertvector(v, b2)); }
; DI float row_rstd(const f32x4 (&v)[4]) {
;     float s = 0.f;
; #pragma unroll
;     for (int j = 0; j < 4; ++j) s += (v[j][0] * v[j][0] + v[j][1] * v[j][1]) + (v[j][2] * v[j][2] + v[j][3] * v[j][3]);
;     return rsqrtf(wave_sum(s) * (1.f / DM) + RMS_EPS);
; DI void phase_ln1(const Args& A, int l, int gw, int ngw, int lane) {
;     ...
;         const float ra = row_rstd(va), rb = row_rstd(vb); uint2* o8a = (uint2*)(hb + (size_t)tok * DM) + lane; uint2* o8b = (uint2*)(hb + (size_t)tokb * DM) + lane;
; #pragma unroll
;         for (int j = 0; j < 4; ++j) { uint2 w; w.x = pkbf(va[j][0] * ra * gg[j][0], va[j][1] * ra * gg[j][1]); w.y = pkbf(va[j][2] * ra * gg[j][2], va[j][3] * ra * gg[j][3]); o8a[64 * j] = w;
;             if (hb2) { uint2 u; u.x = pkbf(vb[j][0] * rb * gg[j][0], vb[j][1] * rb * gg[j][1]); u.y = pkbf(vb[j][2] * rb * gg[j][2], vb[j][3] * rb * gg[j][3]); o8b[64 * j] = u; } }
	v_add_f32_e32 v128, v128, v129
	v_add_f32_e32 v132, v132, v133
	v_add_f32_e32 v136, v136, v137
	v_add_f32_e32 v252, v252, v253
	s_nop 0
	ds_bpermute_b32 v129, v6, v128
	ds_bpermute_b32 v133, v6, v132
	ds_bpermute_b32 v137, v6, v136
	ds_bpermute_b32 v253, v6, v252
	s_waitcnt lgkmcnt(0)
	v_add_f32_e32 v128, v128, v129
	v_add_f32_e32 v132, v132, v133
	v_add_f32_e32 v136, v136, v137
	v_add_f32_e32 v252, v252, v253
	s_nop 0
	ds_bpermute_b32 v129, v7, v128
	ds_bpermute_b32 v133, v7, v132
	ds_bpermute_b32 v137, v7, v136
	ds_bpermute_b32 v253, v7, v252
	s_waitcnt lgkmcnt(0)
	v_add_f32_e32 v128, v128, v129
	v_add_f32_e32 v132, v132, v133
	v_add_f32_e32 v136, v136, v137
	v_add_f32_e32 v252, v252, v253
	s_nop 0
	ds_bpermute_b32 v129, v8, v128
	ds_bpermute_b32 v133, v8, v132
	ds_bpermute_b32 v137, v8, v136
	ds_bpermute_b32 v253, v8, v252
	s_waitcnt lgkmcnt(0)
	v_add_f32_e32 v128, v128, v129
	v_add_f32_e32 v132, v132, v133
	v_add_f32_e32 v136, v136, v137
	v_add_f32_e32 v252, v252, v253
	s_nop 0
	ds_bpermute_b32 v129, v9, v128
	ds_bpermute_b32 v133, v9, v132
	ds_bpermute_b32 v137, v9, v136
	ds_bpermute_b32 v253, v9, v252
	s_waitcnt lgkmcnt(0)
	v_add_f32_e32 v128, v128, v129
	v_add_f32_e32 v132, v132, v133
	v_add_f32_e32 v136, v136, v137
	v_add_f32_e32 v252, v252, v253
	v_fma_f32 v128, v128, s39, v171
	v_mul_f32_e32 v129, 0x4b800000, v128
	v_cmp_gt_f32_e32 vcc, s40, v128
	s_nop 1
	v_cndmask_b32_e32 v128, v128, v129, vcc
	v_rsq_f32_e32 v128, v128
	s_nop 0
	v_mul_f32_e32 v129, 0x45800000, v128
	v_cndmask_b32_e32 v128, v128, v129, vcc
	v_fma_f32 v132, v132, s39, v171
	v_mul_f32_e32 v133, 0x4b800000, v132
	v_cmp_gt_f32_e32 vcc, s40, v132
	s_nop 1
	v_cndmask_b32_e32 v132, v132, v133, vcc
	v_rsq_f32_e32 v132, v132
	s_nop 0
	v_mul_f32_e32 v133, 0x45800000, v132
	v_cndmask_b32_e32 v132, v132, v133, vcc
	v_fma_f32 v136, v136, s39, v171
	v_mul_f32_e32 v137, 0x4b800000, v136
	v_cmp_gt_f32_e32 vcc, s40, v136
	s_nop 1
	v_cndmask_b32_e32 v136, v136, v137, vcc
	v_rsq_f32_e32 v136, v136
	s_nop 0
	v_mul_f32_e32 v137, 0x45800000, v136
	v_cndmask_b32_e32 v136, v136, v137, vcc
	v_fma_f32 v252, v252, s39, v171
	v_mul_f32_e32 v253, 0x4b800000, v252
	v_cmp_gt_f32_e32 vcc, s40, v252
	s_nop 1
	v_cndmask_b32_e32 v252, v252, v253, vcc
	v_rsq_f32_e32 v252, v252
	s_nop 0
	v_mul_f32_e32 v253, 0x45800000, v252
	v_cndmask_b32_e32 v252, v252, v253, vcc
	v_pk_mul_f32 v[172:173], v[172:173], v[128:129] op_sel_hi:[1,0]
	v_pk_mul_f32 v[174:175], v[174:175], v[128:129] op_sel_hi:[1,0]
	v_pk_mul_f32 v[176:177], v[176:177], v[128:129] op_sel_hi:[1,0]
	v_pk_mul_f32 v[178:179], v[178:179], v[128:129] op_sel_hi:[1,0]
	v_pk_mul_f32 v[180:181], v[180:181], v[128:129] op_sel_hi:[1,0]
	v_pk_mul_f32 v[182:183], v[182:183], v[128:129] op_sel_hi:[1,0]
	v_pk_mul_f32 v[184:185], v[184:185], v[128:129] op_sel_hi:[1,0]
	v_pk_mul_f32 v[186:187], v[186:187], v[128:129] op_sel_hi:[1,0]
	v_pk_mul_f32 v[172:173], v[172:173], v[18:19]
	v_pk_mul_f32 v[174:175], v[174:175], v[20:21]
	v_pk_mul_f32 v[176:177], v[176:177], v[22:23]
	v_pk_mul_f32 v[178:179], v[178:179], v[24:25]
	v_pk_mul_f32 v[180:181], v[180:181], v[26:27]
	v_pk_mul_f32 v[182:183], v[182:183], v[28:29]
	v_pk_mul_f32 v[184:185], v[184:185], v[30:31]
	v_pk_mul_f32 v[186:187], v[186:187], v[32:33]
	v_cvt_pk_bf16_f32 v66, v172, v173
	v_cvt_pk_bf16_f32 v67, v174, v175
	v_cvt_pk_bf16_f32 v68, v176, v177
	v_cvt_pk_bf16_f32 v69, v178, v179
	v_cvt_pk_bf16_f32 v70, v180, v181
	v_cvt_pk_bf16_f32 v71, v182, v183
	v_cvt_pk_bf16_f32 v72, v184, v185
	v_cvt_pk_bf16_f32 v73, v186, v187
	s_add_u32 s34, s16, 0x1000000
	s_addc_u32 s35, s17, 0
	global_store_dwordx2 v1, v[66:67], s[34:35]
	global_store_dwordx2 v1, v[68:69], s[34:35] offset:512
	global_store_dwordx2 v1, v[70:71], s[34:35] offset:1024
	global_store_dwordx2 v1, v[72:73], s[34:35] offset:1536
	v_pk_mul_f32 v[188:189], v[188:189], v[132:133] op_sel_hi:[1,0]
	v_pk_mul_f32 v[190:191], v[190:191], v[132:133] op_sel_hi:[1,0]
	v_pk_mul_f32 v[192:193], v[192:193], v[132:133] op_sel_hi:[1,0]
	v_pk_mul_f32 v[194:195], v[194:195], v[132:133] op_sel_hi:[1,0]
	v_pk_mul_f32 v[196:197], v[196:197], v[132:133] op_sel_hi:[1,0]
	v_pk_mul_f32 v[198:199], v[198:199], v[132:133] op_sel_hi:[1,0]
	v_pk_mul_f32 v[200:201], v[200:201], v[132:133] op_sel_hi:[1,0]
	v_pk_mul_f32 v[202:203], v[202:203], v[132:133] op_sel_hi:[1,0]
	v_pk_mul_f32 v[188:189], v[188:189], v[18:19]
	v_pk_mul_f32 v[190:191], v[190:191], v[20:21]
	v_pk_mul_f32 v[192:193], v[192:193], v[22:23]
	v_pk_mul_f32 v[194:195], v[194:195], v[24:25]
	v_pk_mul_f32 v[196:197], v[196:197], v[26:27]
	v_pk_mul_f32 v[198:199], v[198:199], v[28:29]
	v_pk_mul_f32 v[200:201], v[200:201], v[30:31]
	v_pk_mul_f32 v[202:203], v[202:203], v[32:33]
	v_cvt_pk_bf16_f32 v74, v188, v189
	v_cvt_pk_bf16_f32 v75, v190, v191
	v_cvt_pk_bf16_f32 v76, v192, v193
	v_cvt_pk_bf16_f32 v77, v194, v195
	v_cvt_pk_bf16_f32 v78, v196, v197
	v_cvt_pk_bf16_f32 v79, v198, v199
	v_cvt_pk_bf16_f32 v80, v200, v201
	v_cvt_pk_bf16_f32 v81, v202, v203
	s_add_u32 s34, s16, 0x1400000
	s_addc_u32 s35, s17, 0
	global_store_dwordx2 v1, v[74:75], s[34:35]
	global_store_dwordx2 v1, v[76:77], s[34:35] offset:512
; DI unsigned pkbf(float lo, float hi) { typedef __bf16 b2 __attribute__((ext_vector_type(2))); typedef float f2 __attribute__((ext_vector_type(2))); const f2 v = {lo, hi}; return __builtin_bit_cast(unsigned, __builtin_convertvector(v, b2)); }
; DI void phase_ln1(const Args& A, int l, int gw, int ngw, int lane) {
;     const float* xin = A.in[I_X]; const bf16* x1 = (const bf16*)(A.ws + WS_X1); bf16* x2 = (bf16*)(A.ws + WS_X2); bf16* hb = (bf16*)(A.ws + WS_HB);
;     f32x4 gg[4];
; #pragma unroll
;     for (int j = 0; j < 4; ++j) gg[j] = ((const f32x4*)(A.in[I_LN1G] + (size_t)l * DM) + lane)[64 * j];
;     for (int tok = gw; tok < NT; tok += 2 * ngw) {
;         const int tokb = tok + ngw; const bool hb2 = tokb < NT;
;         f32x4 va[4], vb[4];
;         if (l == 0) { load_row(xin + (size_t)tok * DM, lane, va); load_row(xin + (size_t)(hb2 ? tokb : tok) * DM, lane, vb); }
;         else { load_row_bf(x1 + (size_t)tok * DM, lane, va); load_row_bf(x1 + (size_t)(hb2 ? tokb : tok) * DM, lane, vb);
;             add_slots(A, tok, lane, va); add_slots(A, hb2 ? tokb : tok, lane, vb);
;     ...
;         const float ra = row_rstd(va), rb = row_rstd(vb); uint2* o8a = (uint2*)(hb + (size_t)tok * DM) + lane; uint2* o8b = (uint2*)(hb + (size_t)tokb * DM) + lane;
; #pragma unroll
;         for (int j = 0; j < 4; ++j) { uint2 w; w.x = pkbf(va[j][0] * ra * gg[j][0], va[j][1] * ra * gg[j][1]); w.y = pkbf(va[j][2] * ra * gg[j][2], va[j][3] * ra * gg[j][3]); o8a[64 * j] = w;
;             if (hb2) { uint2 u; u.x = pkbf(vb[j][0] * rb * gg[j][0], vb[j][1] * rb * gg[j][1]); u.y = pkbf(vb[j][2] * rb * gg[j][2], vb[j][3] * rb * gg[j][3]); o8b[64 * j] = u; } }
	global_store_dwordx2 v1, v[78:79], s[34:35] offset:1024
	global_store_dwordx2 v1, v[80:81], s[34:35] offset:1536
	v_pk_mul_f32 v[204:205], v[204:205], v[136:137] op_sel_hi:[1,0]
	v_pk_mul_f32 v[206:207], v[206:207], v[136:137] op_sel_hi:[1,0]
	v_pk_mul_f32 v[208:209], v[208:209], v[136:137] op_sel_hi:[1,0]
	v_pk_mul_f32 v[210:211], v[210:211], v[136:137] op_sel_hi:[1,0]
	v_pk_mul_f32 v[212:213], v[212:213], v[136:137] op_sel_hi:[1,0]
	v_pk_mul_f32 v[214:215], v[214:215], v[136:137] op_sel_hi:[1,0]
	v_pk_mul_f32 v[216:217], v[216:217], v[136:137] op_sel_hi:[1,0]
	v_pk_mul_f32 v[218:219], v[218:219], v[136:137] op_sel_hi:[1,0]
	v_pk_mul_f32 v[204:205], v[204:205], v[18:19]
	v_pk_mul_f32 v[206:207], v[206:207], v[20:21]
	v_pk_mul_f32 v[208:209], v[208:209], v[22:23]
	v_pk_mul_f32 v[210:211], v[210:211], v[24:25]
	v_pk_mul_f32 v[212:213], v[212:213], v[26:27]
	v_pk_mul_f32 v[214:215], v[214:215], v[28:29]
	v_pk_mul_f32 v[216:217], v[216:217], v[30:31]
	v_pk_mul_f32 v[218:219], v[218:219], v[32:33]
	v_cvt_pk_bf16_f32 v82, v204, v205
	v_cvt_pk_bf16_f32 v83, v206, v207
	v_cvt_pk_bf16_f32 v84, v208, v209
	v_cvt_pk_bf16_f32 v85, v210, v211
	v_cvt_pk_bf16_f32 v86, v212, v213
	v_cvt_pk_bf16_f32 v87, v214, v215
	v_cvt_pk_bf16_f32 v88, v216, v217
	v_cvt_pk_bf16_f32 v89, v218, v219
	s_add_u32 s34, s16, 0x1800000
	s_addc_u32 s35, s17, 0
	global_store_dwordx2 v1, v[82:83], s[34:35]
	global_store_dwordx2 v1, v[84:85], s[34:35] offset:512
	global_store_dwordx2 v1, v[86:87], s[34:35] offset:1024
	global_store_dwordx2 v1, v[88:89], s[34:35] offset:1536
	v_pk_mul_f32 v[236:237], v[236:237], v[252:253] op_sel_hi:[1,0]
	v_pk_mul_f32 v[238:239], v[238:239], v[252:253] op_sel_hi:[1,0]
	v_pk_mul_f32 v[240:241], v[240:241], v[252:253] op_sel_hi:[1,0]
	v_pk_mul_f32 v[242:243], v[242:243], v[252:253] op_sel_hi:[1,0]
	v_pk_mul_f32 v[244:245], v[244:245], v[252:253] op_sel_hi:[1,0]
	v_pk_mul_f32 v[246:247], v[246:247], v[252:253] op_sel_hi:[1,0]
	v_pk_mul_f32 v[248:249], v[248:249], v[252:253] op_sel_hi:[1,0]
	v_pk_mul_f32 v[250:251], v[250:251], v[252:253] op_sel_hi:[1,0]
	v_pk_mul_f32 v[236:237], v[236:237], v[18:19]
	v_pk_mul_f32 v[238:239], v[238:239], v[20:21]
	v_pk_mul_f32 v[240:241], v[240:241], v[22:23]
	v_pk_mul_f32 v[242:243], v[242:243], v[24:25]
	v_pk_mul_f32 v[244:245], v[244:245], v[26:27]
	v_pk_mul_f32 v[246:247], v[246:247], v[28:29]
	v_pk_mul_f32 v[248:249], v[248:249], v[30:31]
	v_pk_mul_f32 v[250:251], v[250:251], v[32:33]
	v_cvt_pk_bf16_f32 v90, v236, v237
	v_cvt_pk_bf16_f32 v91, v238, v239
	v_cvt_pk_bf16_f32 v92, v240, v241
	v_cvt_pk_bf16_f32 v93, v242, v243
	v_cvt_pk_bf16_f32 v94, v244, v245
	v_cvt_pk_bf16_f32 v95, v246, v247
	v_cvt_pk_bf16_f32 v96, v248, v249
	v_cvt_pk_bf16_f32 v97, v250, v251
	s_add_u32 s34, s16, 0x1c00000
	s_addc_u32 s35, s17, 0
	global_store_dwordx2 v1, v[90:91], s[34:35]
	global_store_dwordx2 v1, v[92:93], s[34:35] offset:512
	global_store_dwordx2 v1, v[94:95], s[34:35] offset:1024
	global_store_dwordx2 v1, v[96:97], s[34:35] offset:1536
	s_branch .LBB0_1578
.Lrw1_orig:
	v_readlane_b32 s12, v235, 17
	s_waitcnt vmcnt(0)
	v_lshlrev_b32_e32 v2, 4, v146
	v_mov_b32_e32 v3, 0
	v_readlane_b32 s16, v235, 21
	v_readlane_b32 s17, v235, 22
	s_mov_b64 s[0:1], 0x1000
	v_mbcnt_lo_u32_b32 v1, -1, 0
	v_lshl_add_u64 v[4:5], s[16:17], 0, v[2:3]
	v_lshl_add_u64 v[6:7], v[4:5], 0, s[0:1]
	v_add_co_u32_e32 v4, vcc, 0x1000, v4
	global_load_dwordx4 v[82:85], v[6:7], off offset:2048
	global_load_dwordx4 v[86:89], v[6:7], off offset:1024
	v_addc_co_u32_e32 v5, vcc, 0, v5, vcc
	global_load_dwordx4 v[90:93], v[6:7], off offset:3072
	global_load_dwordx4 v[94:97], v[4:5], off
	v_lshlrev_b32_e32 v2, 3, v146
	v_lshl_add_u64 v[4:5], s[8:9], 0, v[2:3]
	v_mbcnt_hi_u32_b32 v2, -1, v1
	v_and_b32_e32 v1, 64, v2
	v_xor_b32_e32 v6, 16, v2
	v_add_u32_e32 v7, 64, v1
	v_cmp_lt_i32_e32 vcc, v6, v7
	s_mov_b64 s[0:1], 0x22600000
	v_lshl_add_u64 v[98:99], v[4:5], 0, s[0:1]
	v_cndmask_b32_e32 v6, v2, v6, vcc
	v_lshlrev_b32_e32 v109, 2, v6
	v_xor_b32_e32 v6, 32, v2
	v_cmp_lt_i32_e32 vcc, v6, v7
	s_mov_b64 s[0:1], 0x26600000
	v_lshl_add_u64 v[100:101], v[4:5], 0, s[0:1]
	v_cndmask_b32_e32 v2, v2, v6, vcc
	v_lshlrev_b32_e32 v114, 2, v2
	s_mov_b64 s[0:1], 0x2a600000
	v_lshlrev_b32_e32 v2, 2, v146
	v_lshl_add_u64 v[102:103], v[4:5], 0, s[0:1]
	v_lshl_add_u64 v[2:3], s[8:9], 0, v[2:3]
	s_mov_b64 s[0:1], 0x2c700000
	v_readlane_b32 s13, v235, 18
	v_readlane_b32 s26, v235, 31
	v_lshl_add_u64 v[104:105], v[2:3], 0, s[0:1]
	s_mov_b64 s[0:1], 0x3ba00000
	v_cmp_gt_u32_e64 s[4:5], 16, v146
	s_lshl_b32 s11, s50, 4
	v_lshl_add_u64 v[106:107], v[4:5], 0, s[0:1]
	s_mov_b32 s10, 0x3a800000
	s_mov_b32 s26, 0x800000
	v_mov_b32_e32 v108, 0x358637bd
	v_readlane_b32 s12, v235, 54
	v_readlane_b32 s14, v235, 19
	v_readlane_b32 s15, v235, 20
	v_readlane_b32 s18, v235, 23
	v_readlane_b32 s19, v235, 24
	v_readlane_b32 s20, v235, 25
	v_readlane_b32 s21, v235, 26
	v_readlane_b32 s22, v235, 27
	v_readlane_b32 s23, v235, 28
	v_readlane_b32 s24, v235, 29
	v_readlane_b32 s25, v235, 30
	v_readlane_b32 s27, v235, 32
	v_readlane_b32 s13, v235, 55
	s_branch .LBB0_1522

; DI void add_slots(const Args& A, int tok, int lane, f32x4 (&v)[4]) {
;     const int* sel = (const int*)(A.ws + WS_SEL); const bf16* ys = (const bf16*)(A.ws + WS_YS);
;     const int b = tok / SEQ; const int mys = (lane < NE) ? sel[(size_t)tok * NE + lane] : -1;
;     unsigned m = (unsigned)__ballot(mys >= 0);
; DI void phase_final(const Args& A, int gw, int ngw, int lane) {
;     const bf16* xin = (const bf16*)(A.ws + WS_X1);
;     f32x4 gg[4];
; #pragma unroll
;     for (int j = 0; j < 4; ++j) gg[j] = ((const f32x4*)A.in[I_FG] + lane)[64 * j];
;     for (int tok = gw; tok < NT; tok += 2 * ngw) {
;         const int tokb = tok + ngw; const bool hb2 = tokb < NT;
;         f32x4 va[4], vb[4]; load_row_bf(xin + (size_t)tok * DM, lane, va); load_row_bf(xin + (size_t)(hb2 ? tokb : tok) * DM, lane, vb);
;         add_slots(A, tok, lane, va); add_slots(A, hb2 ? tokb : tok, lane, vb);
.LBB0_2948:
	s_cmp_gt_i32 s6, 21
	s_cselect_b64 s[2:3], -1, 0
	s_xor_b64 s[0:1], s[0:1], -1
	s_or_b64 s[0:1], s[2:3], s[0:1]
	s_and_b64 vcc, exec, s[0:1]
	s_cbranch_vccnz .LBB0_2997
	v_readlane_b32 s0, v234, 42
	v_readlane_b32 s1, v234, 43
	s_andn2_b64 vcc, exec, s[0:1]
	s_cbranch_vccnz .LBB0_2997
	s_cmpk_lg_i32 s50, 0x100
	s_cbranch_scc1 .Lrw2_orig
	s_waitcnt vmcnt(0) lgkmcnt(0)
	v_readlane_b32 s0, v235, 9
	v_readlane_b32 s1, v235, 10
	v_readlane_b32 s18, v235, 54
	v_readlane_b32 s20, v235, 4
	v_readlane_b32 s21, v235, 5
	v_readlane_b32 s14, v235, 6
	v_readlane_b32 s15, v235, 7
	v_lshlrev_b32_e32 v1, 3, v146
	v_lshlrev_b32_e32 v2, 2, v146
	v_lshlrev_b32_e32 v3, 4, v146
	v_xor_b32_e32 v4, 1, v146
	v_lshlrev_b32_e32 v4, 2, v4
	v_xor_b32_e32 v5, 2, v146
	v_lshlrev_b32_e32 v5, 2, v5
	v_xor_b32_e32 v6, 4, v146
	v_lshlrev_b32_e32 v6, 2, v6
	v_xor_b32_e32 v7, 8, v146
	v_lshlrev_b32_e32 v7, 2, v7
	v_xor_b32_e32 v8, 16, v146
	v_lshlrev_b32_e32 v8, 2, v8
	v_xor_b32_e32 v9, 32, v146
	v_lshlrev_b32_e32 v9, 2, v9
	v_mov_b32_e32 v171, 0x358637bd
	s_mov_b32 s39, 0x3a800000
	s_mov_b32 s40, 0x800000
	s_lshl_b32 s19, s18, 11
	s_add_u32 s4, s0, 0x22600000
	s_addc_u32 s5, s1, 0
	s_add_u32 s4, s4, s19
	s_addc_u32 s5, s5, 0
	s_lshl_b32 s34, s18, 6
	s_add_u32 s6, s0, 0x2c700000
	s_addc_u32 s7, s1, 0
	s_add_u32 s6, s6, s34
	s_addc_u32 s7, s7, 0
	s_add_u32 s12, s0, 0x3ba00000
	s_addc_u32 s13, s1, 0
	s_lshl_b32 s34, s18, 12
	s_add_u32 s14, s14, s34
	s_addc_u32 s15, s15, 0
	v_mov_b32_e32 v10, -1
	v_mov_b32_e32 v11, -1
	v_mov_b32_e32 v12, -1
	v_mov_b32_e32 v13, -1
	v_mov_b32_e32 v14, -1
	v_mov_b32_e32 v15, -1
	v_mov_b32_e32 v16, -1
	v_mov_b32_e32 v17, -1
	s_mov_b64 exec, 0xffff
	s_mov_b64 s[34:35], s[6:7]
	global_load_dword v10, v2, s[34:35]
	s_add_u32 s34, s6, 0x20000
	s_addc_u32 s35, s7, 0
	global_load_dword v11, v2, s[34:35]
	s_add_u32 s34, s6, 0x40000
	s_addc_u32 s35, s7, 0
	global_load_dword v12, v2, s[34:35]
	s_add_u32 s34, s6, 0x60000
	s_addc_u32 s35, s7, 0
	global_load_dword v13, v2, s[34:35]
	s_add_u32 s34, s6, 0x80000
	s_addc_u32 s35, s7, 0
	global_load_dword v14, v2, s[34:35]
	s_add_u32 s34, s6, 0xa0000
	s_addc_u32 s35, s7, 0
	global_load_dword v15, v2, s[34:35]
	s_add_u32 s34, s6, 0xc0000
	s_addc_u32 s35, s7, 0
	global_load_dword v16, v2, s[34:35]
	s_add_u32 s34, s6, 0xe0000
	s_addc_u32 s35, s7, 0
	global_load_dword v17, v2, s[34:35]
	s_mov_b64 exec, -1
	s_mov_b64 s[34:35], s[4:5]
	global_load_dwordx2 v[34:35], v1, s[34:35]
	global_load_dwordx2 v[36:37], v1, s[34:35] offset:512
	global_load_dwordx2 v[38:39], v1, s[34:35] offset:1024
	global_load_dwordx2 v[40:41], v1, s[34:35] offset:1536
	s_add_u32 s34, s4, 0x400000
	s_addc_u32 s35, s5, 0
	global_load_dwordx2 v[42:43], v1, s[34:35]
	global_load_dwordx2 v[44:45], v1, s[34:35] offset:512
	global_load_dwordx2 v[46:47], v1, s[34:35] offset:1024
	global_load_dwordx2 v[48:49], v1, s[34:35] offset:1536
	s_add_u32 s34, s4, 0x800000
	s_addc_u32 s35, s5, 0
	global_load_dwordx2 v[50:51], v1, s[34:35]
	global_load_dwordx2 v[52:53], v1, s[34:35] offset:512
	global_load_dwordx2 v[54:55], v1, s[34:35] offset:1024
	global_load_dwordx2 v[56:57], v1, s[34:35] offset:1536
	s_add_u32 s34, s4, 0xc00000
	s_addc_u32 s35, s5, 0
	global_load_dwordx2 v[58:59], v1, s[34:35]
	global_load_dwordx2 v[60:61], v1, s[34:35] offset:512
	global_load_dwordx2 v[62:63], v1, s[34:35] offset:1024
	global_load_dwordx2 v[64:65], v1, s[34:35] offset:1536
	s_add_u32 s34, s4, 0x1000000
	s_addc_u32 s35, s5, 0
	global_load_dwordx2 v[66:67], v1, s[34:35]
	global_load_dwordx2 v[68:69], v1, s[34:35] offset:512
	global_load_dwordx2 v[70:71], v1, s[34:35] offset:1024
	global_load_dwordx2 v[72:73], v1, s[34:35] offset:1536
	s_add_u32 s34, s4, 0x1400000
	s_addc_u32 s35, s5, 0
	global_load_dwordx2 v[74:75], v1, s[34:35]
	global_load_dwordx2 v[76:77], v1, s[34:35] offset:512
	global_load_dwordx2 v[78:79], v1, s[34:35] offset:1024
	global_load_dwordx2 v[80:81], v1, s[34:35] offset:1536
	s_add_u32 s34, s4, 0x1800000
	s_addc_u32 s35, s5, 0
	global_load_dwordx2 v[82:83], v1, s[34:35]
	global_load_dwordx2 v[84:85], v1, s[34:35] offset:512
	global_load_dwordx2 v[86:87], v1, s[34:35] offset:1024
	global_load_dwordx2 v[88:89], v1, s[34:35] offset:1536
	s_add_u32 s34, s4, 0x1c00000
	s_addc_u32 s35, s5, 0
	global_load_dwordx2 v[90:91], v1, s[34:35]
	global_load_dwordx2 v[92:93], v1, s[34:35] offset:512
	global_load_dwordx2 v[94:95], v1, s[34:35] offset:1024
	global_load_dwordx2 v[96:97], v1, s[34:35] offset:1536
	global_load_dwordx4 v[18:21], v3, s[20:21]
	global_load_dwordx4 v[22:25], v3, s[20:21] offset:1024
	global_load_dwordx4 v[26:29], v3, s[20:21] offset:2048
	global_load_dwordx4 v[30:33], v3, s[20:21] offset:3072
	s_waitcnt vmcnt(36)
	v_cmp_le_i32_e64 s[66:67], 0, v10
	v_cmp_le_i32_e64 s[68:69], 0, v11
	v_cmp_le_i32_e64 s[70:71], 0, v12
	v_cmp_le_i32_e64 s[72:73], 0, v13
	v_cmp_le_i32_e64 s[74:75], 0, v14
	v_cmp_le_i32_e64 s[76:77], 0, v15
	v_cmp_le_i32_e64 s[78:79], 0, v16
	v_cmp_le_i32_e64 s[80:81], 0, v17
	s_nop 1
	s_mov_b32 s38, 1

; #define DPPF(v, ctrl) __uint_as_float((unsigned)__builtin_amdgcn_update_dpp(0, (int)__float_as_uint(v), (ctrl), 0xf, 0xf, true))
; DI float row16_sum(float v) { v += DPPF(v, 0xB1); v += DPPF(v, 0x4E); v += DPPF(v, 0x141); v += DPPF(v, 0x140); return v; }
; DI float wave_sum(float v) { v = row16_sum(v); v += __shfl_xor(v, 16); v += __shfl_xor(v, 32); return v; }
; DI float row_rstd(const f32x4 (&v)[4]) {
;     float s = 0.f;
; #pragma unroll
;     for (int j = 0; j < 4; ++j) s += (v[j][0] * v[j][0] + v[j][1] * v[j][1]) + (v[j][2] * v[j][2] + v[j][3] * v[j][3]);
;     return rsqrtf(wave_sum(s) * (1.f / DM) + RMS_EPS);
; }
.Lrw2_a0_7:
	s_or_b32 s34, s66, s68
	s_or_b32 s34, s34, s70
	s_or_b32 s34, s34, s72
	s_cmp_lg_u32 s34, 0
	s_cbranch_scc1 .Lrw2_round0
	v_mul_f32_e32 v128, v172, v172
	v_mul_f32_e32 v129, v174, v174
	v_fmac_f32_e32 v128, v173, v173
	v_fmac_f32_e32 v129, v175, v175
	v_add_f32_e32 v128, v128, v129
	v_mul_f32_e32 v132, v188, v188
	v_mul_f32_e32 v133, v190, v190
	v_fmac_f32_e32 v132, v189, v189
	v_fmac_f32_e32 v133, v191, v191
	v_add_f32_e32 v132, v132, v133
	v_mul_f32_e32 v136, v204, v204
	v_mul_f32_e32 v137, v206, v206
	v_fmac_f32_e32 v136, v205, v205
	v_fmac_f32_e32 v137, v207, v207
	v_add_f32_e32 v136, v136, v137
	v_mul_f32_e32 v252, v236, v236
	v_mul_f32_e32 v253, v238, v238
	v_fmac_f32_e32 v252, v237, v237
	v_fmac_f32_e32 v253, v239, v239
	v_add_f32_e32 v252, v252, v253
	v_mul_f32_e32 v129, v176, v176
	v_mul_f32_e32 v254, v178, v178
	v_fmac_f32_e32 v129, v177, v177
	v_fmac_f32_e32 v254, v179, v179
	v_add_f32_e32 v129, v129, v254
	v_add_f32_e32 v128, v128, v129
	v_mul_f32_e32 v133, v192, v192
	v_mul_f32_e32 v255, v194, v194
	v_fmac_f32_e32 v133, v193, v193
	v_fmac_f32_e32 v255, v195, v195
	v_add_f32_e32 v133, v133, v255
	v_add_f32_e32 v132, v132, v133
	v_mul_f32_e32 v137, v208, v208
	v_mul_f32_e32 v254, v210, v210
	v_fmac_f32_e32 v137, v209, v209
	v_fmac_f32_e32 v254, v211, v211
	v_add_f32_e32 v137, v137, v254
	v_add_f32_e32 v136, v136, v137
	v_mul_f32_e32 v253, v240, v240
	v_mul_f32_e32 v255, v242, v242
	v_fmac_f32_e32 v253, v241, v241
	v_fmac_f32_e32 v255, v243, v243
	v_add_f32_e32 v253, v253, v255
	v_add_f32_e32 v252, v252, v253
	v_mul_f32_e32 v129, v180, v180
	v_mul_f32_e32 v254, v182, v182
	v_fmac_f32_e32 v129, v181, v181
	v_fmac_f32_e32 v254, v183, v183
	v_add_f32_e32 v129, v129, v254
	v_add_f32_e32 v128, v128, v129
	v_mul_f32_e32 v133, v196, v196
	v_mul_f32_e32 v255, v198, v198
	v_fmac_f32_e32 v133, v197, v197
	v_fmac_f32_e32 v255, v199, v199
	v_add_f32_e32 v133, v133, v255
	v_add_f32_e32 v132, v132, v133
	v_mul_f32_e32 v137, v212, v212
	v_mul_f32_e32 v254, v214, v214
	v_fmac_f32_e32 v137, v213, v213
	v_fmac_f32_e32 v254, v215, v215
	v_add_f32_e32 v137, v137, v254
	v_add_f32_e32 v136, v136, v137
	v_mul_f32_e32 v253, v244, v244
	v_mul_f32_e32 v255, v246, v246
	v_fmac_f32_e32 v253, v245, v245
	v_fmac_f32_e32 v255, v247, v247
	v_add_f32_e32 v253, v253, v255
	v_add_f32_e32 v252, v252, v253
	v_mul_f32_e32 v129, v184, v184
	v_mul_f32_e32 v254, v186, v186
	v_fmac_f32_e32 v129, v185, v185
	v_fmac_f32_e32 v254, v187, v187
	v_add_f32_e32 v129, v129, v254
	v_add_f32_e32 v128, v128, v129
	v_mul_f32_e32 v133, v200, v200
	v_mul_f32_e32 v255, v202, v202
	v_fmac_f32_e32 v133, v201, v201
	v_fmac_f32_e32 v255, v203, v203
	v_add_f32_e32 v133, v133, v255
	v_add_f32_e32 v132, v132, v133
	v_mul_f32_e32 v137, v216, v216
	v_mul_f32_e32 v254, v218, v218
	v_fmac_f32_e32 v137, v217, v217
	v_fmac_f32_e32 v254, v219, v219
	v_add_f32_e32 v137, v137, v254
	v_add_f32_e32 v136, v136, v137
	v_mul_f32_e32 v253, v248, v248
	v_mul_f32_e32 v255, v250, v250
	v_fmac_f32_e32 v253, v249, v249
	v_fmac_f32_e32 v255, v251, v251
	v_add_f32_e32 v253, v253, v255
	v_add_f32_e32 v252, v252, v253
	s_nop 0
	ds_bpermute_b32 v129, v4, v128
	ds_bpermute_b32 v133, v4, v132
	ds_bpermute_b32 v137, v4, v136
	ds_bpermute_b32 v253, v4, v252
	s_waitcnt lgkmcnt(0)
	v_add_f32_e32 v128, v128, v129
	v_add_f32_e32 v132, v132, v133
	v_add_f32_e32 v136, v136, v137
	v_add_f32_e32 v252, v252, v253
	s_nop 0
	ds_bpermute_b32 v129, v5, v128
	ds_bpermute_b32 v133, v5, v132
	ds_bpermute_b32 v137, v5, v136
	ds_bpermute_b32 v253, v5, v252
	s_waitcnt lgkmcnt(0)
	v_add_f32_e32 v128, v128, v129
	v_add_f32_e32 v132, v132, v133
	v_add_f32_e32 v136, v136, v137
	v_add_f32_e32 v252, v252, v253
	s_nop 0
	ds_bpermute_b32 v129, v6, v128
	ds_bpermute_b32 v133, v6, v132
	ds_bpermute_b32 v137, v6, v136
	ds_bpermute_b32 v253, v6, v252
	s_waitcnt lgkmcnt(0)
	v_add_f32_e32 v128, v128, v129
	v_add_f32_e32 v132, v132, v133
	v_add_f32_e32 v136, v136, v137
	v_add_f32_e32 v252, v252, v253
	s_nop 0
	ds_bpermute_b32 v129, v7, v128
	ds_bpermute_b32 v133, v7, v132
	ds_bpermute_b32 v137, v7, v136
	ds_bpermute_b32 v253, v7, v252
	s_waitcnt lgkmcnt(0)
	v_add_f32_e32 v128, v128, v129
	v_add_f32_e32 v132, v132, v133
	v_add_f32_e32 v136, v136, v137
	v_add_f32_e32 v252, v252, v253
	s_nop 0
	ds_bpermute_b32 v129, v8, v128
	ds_bpermute_b32 v133, v8, v132
	ds_bpermute_b32 v137, v8, v136
	ds_bpermute_b32 v253, v8, v252
	s_waitcnt lgkmcnt(0)
	v_add_f32_e32 v128, v128, v129
	v_add_f32_e32 v132, v132, v133
	v_add_f32_e32 v136, v136, v137
	v_add_f32_e32 v252, v252, v253
	s_nop 0
	ds_bpermute_b32 v129, v9, v128
	ds_bpermute_b32 v133, v9, v132
	ds_bpermute_b32 v137, v9, v136
	ds_bpermute_b32 v253, v9, v252
	s_waitcnt lgkmcnt(0)
; DI float wave_sum(float v) { v = row16_sum(v); v += __shfl_xor(v, 16); v += __shfl_xor(v, 32); return v; }
; DI float row_rstd(const f32x4 (&v)[4]) {
;     float s = 0.f;
; #pragma unroll
;     for (int j = 0; j < 4; ++j) s += (v[j][0] * v[j][0] + v[j][1] * v[j][1]) + (v[j][2] * v[j][2] + v[j][3] * v[j][3]);
;     return rsqrtf(wave_sum(s) * (1.f / DM) + RMS_EPS);
; DI void phase_final(const Args& A, int gw, int ngw, int lane) {
;     ...
;         const float ra = row_rstd(va), rb = row_rstd(vb); f32x4* oa = (f32x4*)(A.out + (size_t)tok * DM) + lane; f32x4* ob = (f32x4*)(A.out + (size_t)tokb * DM) + lane;
; #pragma unroll
;         for (int j = 0; j < 4; ++j) { oa[64 * j] = va[j] * ra * gg[j]; if (hb2) ob[64 * j] = vb[j] * rb * gg[j]; }
	v_add_f32_e32 v128, v128, v129
	v_add_f32_e32 v132, v132, v133
	v_add_f32_e32 v136, v136, v137
	v_add_f32_e32 v252, v252, v253
	v_fma_f32 v128, v128, s39, v171
	v_mul_f32_e32 v129, 0x4b800000, v128
	v_cmp_gt_f32_e32 vcc, s40, v128
	s_nop 1
	v_cndmask_b32_e32 v128, v128, v129, vcc
	v_rsq_f32_e32 v128, v128
	s_nop 0
	v_mul_f32_e32 v129, 0x45800000, v128
	v_cndmask_b32_e32 v128, v128, v129, vcc
	v_fma_f32 v132, v132, s39, v171
	v_mul_f32_e32 v133, 0x4b800000, v132
	v_cmp_gt_f32_e32 vcc, s40, v132
	s_nop 1
	v_cndmask_b32_e32 v132, v132, v133, vcc
	v_rsq_f32_e32 v132, v132
	s_nop 0
	v_mul_f32_e32 v133, 0x45800000, v132
	v_cndmask_b32_e32 v132, v132, v133, vcc
	v_fma_f32 v136, v136, s39, v171
	v_mul_f32_e32 v137, 0x4b800000, v136
	v_cmp_gt_f32_e32 vcc, s40, v136
	s_nop 1
	v_cndmask_b32_e32 v136, v136, v137, vcc
	v_rsq_f32_e32 v136, v136
	s_nop 0
	v_mul_f32_e32 v137, 0x45800000, v136
	v_cndmask_b32_e32 v136, v136, v137, vcc
	v_fma_f32 v252, v252, s39, v171
	v_mul_f32_e32 v253, 0x4b800000, v252
	v_cmp_gt_f32_e32 vcc, s40, v252
	s_nop 1
	v_cndmask_b32_e32 v252, v252, v253, vcc
	v_rsq_f32_e32 v252, v252
	s_nop 0
	v_mul_f32_e32 v253, 0x45800000, v252
	v_cndmask_b32_e32 v252, v252, v253, vcc
	v_pk_mul_f32 v[172:173], v[172:173], v[128:129] op_sel_hi:[1,0]
	v_pk_mul_f32 v[174:175], v[174:175], v[128:129] op_sel_hi:[1,0]
	v_pk_mul_f32 v[176:177], v[176:177], v[128:129] op_sel_hi:[1,0]
	v_pk_mul_f32 v[178:179], v[178:179], v[128:129] op_sel_hi:[1,0]
	v_pk_mul_f32 v[180:181], v[180:181], v[128:129] op_sel_hi:[1,0]
	v_pk_mul_f32 v[182:183], v[182:183], v[128:129] op_sel_hi:[1,0]
	v_pk_mul_f32 v[184:185], v[184:185], v[128:129] op_sel_hi:[1,0]
	v_pk_mul_f32 v[186:187], v[186:187], v[128:129] op_sel_hi:[1,0]
	v_pk_mul_f32 v[172:173], v[172:173], v[18:19]
	v_pk_mul_f32 v[174:175], v[174:175], v[20:21]
	v_pk_mul_f32 v[176:177], v[176:177], v[22:23]
	v_pk_mul_f32 v[178:179], v[178:179], v[24:25]
	v_pk_mul_f32 v[180:181], v[180:181], v[26:27]
	v_pk_mul_f32 v[182:183], v[182:183], v[28:29]
	v_pk_mul_f32 v[184:185], v[184:185], v[30:31]
	v_pk_mul_f32 v[186:187], v[186:187], v[32:33]
	s_mov_b64 s[34:35], s[14:15]
	global_store_dwordx4 v3, v[172:175], s[34:35]
	global_store_dwordx4 v3, v[176:179], s[34:35] offset:1024
	global_store_dwordx4 v3, v[180:183], s[34:35] offset:2048
	global_store_dwordx4 v3, v[184:187], s[34:35] offset:3072
	v_pk_mul_f32 v[188:189], v[188:189], v[132:133] op_sel_hi:[1,0]
	v_pk_mul_f32 v[190:191], v[190:191], v[132:133] op_sel_hi:[1,0]
	v_pk_mul_f32 v[192:193], v[192:193], v[132:133] op_sel_hi:[1,0]
	v_pk_mul_f32 v[194:195], v[194:195], v[132:133] op_sel_hi:[1,0]
	v_pk_mul_f32 v[196:197], v[196:197], v[132:133] op_sel_hi:[1,0]
	v_pk_mul_f32 v[198:199], v[198:199], v[132:133] op_sel_hi:[1,0]
	v_pk_mul_f32 v[200:201], v[200:201], v[132:133] op_sel_hi:[1,0]
	v_pk_mul_f32 v[202:203], v[202:203], v[132:133] op_sel_hi:[1,0]
	v_pk_mul_f32 v[188:189], v[188:189], v[18:19]
	v_pk_mul_f32 v[190:191], v[190:191], v[20:21]
	v_pk_mul_f32 v[192:193], v[192:193], v[22:23]
	v_pk_mul_f32 v[194:195], v[194:195], v[24:25]
	v_pk_mul_f32 v[196:197], v[196:197], v[26:27]
	v_pk_mul_f32 v[198:199], v[198:199], v[28:29]
	v_pk_mul_f32 v[200:201], v[200:201], v[30:31]
	v_pk_mul_f32 v[202:203], v[202:203], v[32:33]
	s_add_u32 s34, s14, 0x800000
	s_addc_u32 s35, s15, 0
	global_store_dwordx4 v3, v[188:191], s[34:35]
	global_store_dwordx4 v3, v[192:195], s[34:35] offset:1024
	global_store_dwordx4 v3, v[196:199], s[34:35] offset:2048
	global_store_dwordx4 v3, v[200:203], s[34:35] offset:3072
	v_pk_mul_f32 v[204:205], v[204:205], v[136:137] op_sel_hi:[1,0]
	v_pk_mul_f32 v[206:207], v[206:207], v[136:137] op_sel_hi:[1,0]
	v_pk_mul_f32 v[208:209], v[208:209], v[136:137] op_sel_hi:[1,0]
	v_pk_mul_f32 v[210:211], v[210:211], v[136:137] op_sel_hi:[1,0]
	v_pk_mul_f32 v[212:213], v[212:213], v[136:137] op_sel_hi:[1,0]
	v_pk_mul_f32 v[214:215], v[214:215], v[136:137] op_sel_hi:[1,0]
	v_pk_mul_f32 v[216:217], v[216:217], v[136:137] op_sel_hi:[1,0]
	v_pk_mul_f32 v[218:219], v[218:219], v[136:137] op_sel_hi:[1,0]
	v_pk_mul_f32 v[204:205], v[204:205], v[18:19]
	v_pk_mul_f32 v[206:207], v[206:207], v[20:21]
	v_pk_mul_f32 v[208:209], v[208:209], v[22:23]
	v_pk_mul_f32 v[210:211], v[210:211], v[24:25]
	v_pk_mul_f32 v[212:213], v[212:213], v[26:27]
	v_pk_mul_f32 v[214:215], v[214:215], v[28:29]
	v_pk_mul_f32 v[216:217], v[216:217], v[30:31]
	v_pk_mul_f32 v[218:219], v[218:219], v[32:33]
	s_add_u32 s34, s14, 0x1000000
	s_addc_u32 s35, s15, 0
	global_store_dwordx4 v3, v[204:207], s[34:35]
	global_store_dwordx4 v3, v[208:211], s[34:35] offset:1024
	global_store_dwordx4 v3, v[212:215], s[34:35] offset:2048
	global_store_dwordx4 v3, v[216:219], s[34:35] offset:3072
	v_pk_mul_f32 v[236:237], v[236:237], v[252:253] op_sel_hi:[1,0]
	v_pk_mul_f32 v[238:239], v[238:239], v[252:253] op_sel_hi:[1,0]
	v_pk_mul_f32 v[240:241], v[240:241], v[252:253] op_sel_hi:[1,0]
	v_pk_mul_f32 v[242:243], v[242:243], v[252:253] op_sel_hi:[1,0]
	v_pk_mul_f32 v[244:245], v[244:245], v[252:253] op_sel_hi:[1,0]
	v_pk_mul_f32 v[246:247], v[246:247], v[252:253] op_sel_hi:[1,0]
	v_pk_mul_f32 v[248:249], v[248:249], v[252:253] op_sel_hi:[1,0]
	v_pk_mul_f32 v[250:251], v[250:251], v[252:253] op_sel_hi:[1,0]
	v_pk_mul_f32 v[236:237], v[236:237], v[18:19]
	v_pk_mul_f32 v[238:239], v[238:239], v[20:21]
	v_pk_mul_f32 v[240:241], v[240:241], v[22:23]
	v_pk_mul_f32 v[242:243], v[242:243], v[24:25]
	v_pk_mul_f32 v[244:245], v[244:245], v[26:27]
	v_pk_mul_f32 v[246:247], v[246:247], v[28:29]
	v_pk_mul_f32 v[248:249], v[248:249], v[30:31]
	v_pk_mul_f32 v[250:251], v[250:251], v[32:33]
	s_add_u32 s34, s14, 0x1800000
	s_addc_u32 s35, s15, 0
	global_store_dwordx4 v3, v[236:239], s[34:35]
	global_store_dwordx4 v3, v[240:243], s[34:35] offset:1024
	global_store_dwordx4 v3, v[244:247], s[34:35] offset:2048
	global_store_dwordx4 v3, v[248:251], s[34:35] offset:3072
	s_mov_b32 s38, 1

; #define DPPF(v, ctrl) __uint_as_float((unsigned)__builtin_amdgcn_update_dpp(0, (int)__float_as_uint(v), (ctrl), 0xf, 0xf, true))
; DI float row16_sum(float v) { v += DPPF(v, 0xB1); v += DPPF(v, 0x4E); v += DPPF(v, 0x141); v += DPPF(v, 0x140); return v; }
; DI float wave_sum(float v) { v = row16_sum(v); v += __shfl_xor(v, 16); v += __shfl_xor(v, 32); return v; }
; DI float row_rstd(const f32x4 (&v)[4]) {
;     float s = 0.f;
; #pragma unroll
;     for (int j = 0; j < 4; ++j) s += (v[j][0] * v[j][0] + v[j][1] * v[j][1]) + (v[j][2] * v[j][2] + v[j][3] * v[j][3]);
;     return rsqrtf(wave_sum(s) * (1.f / DM) + RMS_EPS);
; }
.Lrw2_a1_7:
	s_or_b32 s34, s74, s76
	s_or_b32 s34, s34, s78
	s_or_b32 s34, s34, s80
	s_cmp_lg_u32 s34, 0
	s_cbranch_scc1 .Lrw2_round1
	v_mul_f32_e32 v128, v172, v172
	v_mul_f32_e32 v129, v174, v174
	v_fmac_f32_e32 v128, v173, v173
	v_fmac_f32_e32 v129, v175, v175
	v_add_f32_e32 v128, v128, v129
	v_mul_f32_e32 v132, v188, v188
	v_mul_f32_e32 v133, v190, v190
	v_fmac_f32_e32 v132, v189, v189
	v_fmac_f32_e32 v133, v191, v191
	v_add_f32_e32 v132, v132, v133
	v_mul_f32_e32 v136, v204, v204
	v_mul_f32_e32 v137, v206, v206
	v_fmac_f32_e32 v136, v205, v205
	v_fmac_f32_e32 v137, v207, v207
	v_add_f32_e32 v136, v136, v137
	v_mul_f32_e32 v252, v236, v236
	v_mul_f32_e32 v253, v238, v238
	v_fmac_f32_e32 v252, v237, v237
	v_fmac_f32_e32 v253, v239, v239
	v_add_f32_e32 v252, v252, v253
	v_mul_f32_e32 v129, v176, v176
	v_mul_f32_e32 v254, v178, v178
	v_fmac_f32_e32 v129, v177, v177
	v_fmac_f32_e32 v254, v179, v179
	v_add_f32_e32 v129, v129, v254
	v_add_f32_e32 v128, v128, v129
	v_mul_f32_e32 v133, v192, v192
	v_mul_f32_e32 v255, v194, v194
	v_fmac_f32_e32 v133, v193, v193
	v_fmac_f32_e32 v255, v195, v195
	v_add_f32_e32 v133, v133, v255
	v_add_f32_e32 v132, v132, v133
	v_mul_f32_e32 v137, v208, v208
	v_mul_f32_e32 v254, v210, v210
	v_fmac_f32_e32 v137, v209, v209
	v_fmac_f32_e32 v254, v211, v211
	v_add_f32_e32 v137, v137, v254
	v_add_f32_e32 v136, v136, v137
	v_mul_f32_e32 v253, v240, v240
	v_mul_f32_e32 v255, v242, v242
	v_fmac_f32_e32 v253, v241, v241
	v_fmac_f32_e32 v255, v243, v243
	v_add_f32_e32 v253, v253, v255
	v_add_f32_e32 v252, v252, v253
	v_mul_f32_e32 v129, v180, v180
	v_mul_f32_e32 v254, v182, v182
	v_fmac_f32_e32 v129, v181, v181
	v_fmac_f32_e32 v254, v183, v183
	v_add_f32_e32 v129, v129, v254
	v_add_f32_e32 v128, v128, v129
	v_mul_f32_e32 v133, v196, v196
	v_mul_f32_e32 v255, v198, v198
	v_fmac_f32_e32 v133, v197, v197
	v_fmac_f32_e32 v255, v199, v199
	v_add_f32_e32 v133, v133, v255
	v_add_f32_e32 v132, v132, v133
	v_mul_f32_e32 v137, v212, v212
	v_mul_f32_e32 v254, v214, v214
	v_fmac_f32_e32 v137, v213, v213
	v_fmac_f32_e32 v254, v215, v215
	v_add_f32_e32 v137, v137, v254
	v_add_f32_e32 v136, v136, v137
	v_mul_f32_e32 v253, v244, v244
	v_mul_f32_e32 v255, v246, v246
	v_fmac_f32_e32 v253, v245, v245
	v_fmac_f32_e32 v255, v247, v247
	v_add_f32_e32 v253, v253, v255
	v_add_f32_e32 v252, v252, v253
	v_mul_f32_e32 v129, v184, v184
	v_mul_f32_e32 v254, v186, v186
	v_fmac_f32_e32 v129, v185, v185
	v_fmac_f32_e32 v254, v187, v187
	v_add_f32_e32 v129, v129, v254
	v_add_f32_e32 v128, v128, v129
	v_mul_f32_e32 v133, v200, v200
	v_mul_f32_e32 v255, v202, v202
	v_fmac_f32_e32 v133, v201, v201
	v_fmac_f32_e32 v255, v203, v203
	v_add_f32_e32 v133, v133, v255
	v_add_f32_e32 v132, v132, v133
	v_mul_f32_e32 v137, v216, v216
	v_mul_f32_e32 v254, v218, v218
	v_fmac_f32_e32 v137, v217, v217
	v_fmac_f32_e32 v254, v219, v219
	v_add_f32_e32 v137, v137, v254
	v_add_f32_e32 v136, v136, v137
	v_mul_f32_e32 v253, v248, v248
	v_mul_f32_e32 v255, v250, v250
	v_fmac_f32_e32 v253, v249, v249
	v_fmac_f32_e32 v255, v251, v251
	v_add_f32_e32 v253, v253, v255
	v_add_f32_e32 v252, v252, v253
	s_nop 0
	ds_bpermute_b32 v129, v4, v128
	ds_bpermute_b32 v133, v4, v132
	ds_bpermute_b32 v137, v4, v136
	ds_bpermute_b32 v253, v4, v252
	s_waitcnt lgkmcnt(0)
	v_add_f32_e32 v128, v128, v129
	v_add_f32_e32 v132, v132, v133
	v_add_f32_e32 v136, v136, v137
	v_add_f32_e32 v252, v252, v253
	s_nop 0
	ds_bpermute_b32 v129, v5, v128
	ds_bpermute_b32 v133, v5, v132
	ds_bpermute_b32 v137, v5, v136
	ds_bpermute_b32 v253, v5, v252
	s_waitcnt lgkmcnt(0)
	v_add_f32_e32 v128, v128, v129
	v_add_f32_e32 v132, v132, v133
	v_add_f32_e32 v136, v136, v137
	v_add_f32_e32 v252, v252, v253
	s_nop 0
	ds_bpermute_b32 v129, v6, v128
	ds_bpermute_b32 v133, v6, v132
	ds_bpermute_b32 v137, v6, v136
	ds_bpermute_b32 v253, v6, v252
	s_waitcnt lgkmcnt(0)
	v_add_f32_e32 v128, v128, v129
	v_add_f32_e32 v132, v132, v133
	v_add_f32_e32 v136, v136, v137
	v_add_f32_e32 v252, v252, v253
	s_nop 0
	ds_bpermute_b32 v129, v7, v128
	ds_bpermute_b32 v133, v7, v132
	ds_bpermute_b32 v137, v7, v136
	ds_bpermute_b32 v253, v7, v252
	s_waitcnt lgkmcnt(0)
	v_add_f32_e32 v128, v128, v129
	v_add_f32_e32 v132, v132, v133
	v_add_f32_e32 v136, v136, v137
	v_add_f32_e32 v252, v252, v253
	s_nop 0
	ds_bpermute_b32 v129, v8, v128
	ds_bpermute_b32 v133, v8, v132
	ds_bpermute_b32 v137, v8, v136
	ds_bpermute_b32 v253, v8, v252
	s_waitcnt lgkmcnt(0)
	v_add_f32_e32 v128, v128, v129
	v_add_f32_e32 v132, v132, v133
	v_add_f32_e32 v136, v136, v137
	v_add_f32_e32 v252, v252, v253
	s_nop 0
	ds_bpermute_b32 v129, v9, v128
	ds_bpermute_b32 v133, v9, v132
	ds_bpermute_b32 v137, v9, v136
	ds_bpermute_b32 v253, v9, v252
	s_waitcnt lgkmcnt(0)
; DI float wave_sum(float v) { v = row16_sum(v); v += __shfl_xor(v, 16); v += __shfl_xor(v, 32); return v; }
; DI float row_rstd(const f32x4 (&v)[4]) {
;     float s = 0.f;
; #pragma unroll
;     for (int j = 0; j < 4; ++j) s += (v[j][0] * v[j][0] + v[j][1] * v[j][1]) + (v[j][2] * v[j][2] + v[j][3] * v[j][3]);
;     return rsqrtf(wave_sum(s) * (1.f / DM) + RMS_EPS);
; DI void phase_final(const Args& A, int gw, int ngw, int lane) {
;     ...
;         const float ra = row_rstd(va), rb = row_rstd(vb); f32x4* oa = (f32x4*)(A.out + (size_t)tok * DM) + lane; f32x4* ob = (f32x4*)(A.out + (size_t)tokb * DM) + lane;
; #pragma unroll
;         for (int j = 0; j < 4; ++j) { oa[64 * j] = va[j] * ra * gg[j]; if (hb2) ob[64 * j] = vb[j] * rb * gg[j]; }
	v_add_f32_e32 v128, v128, v129
	v_add_f32_e32 v132, v132, v133
	v_add_f32_e32 v136, v136, v137
	v_add_f32_e32 v252, v252, v253
	v_fma_f32 v128, v128, s39, v171
	v_mul_f32_e32 v129, 0x4b800000, v128
	v_cmp_gt_f32_e32 vcc, s40, v128
	s_nop 1
	v_cndmask_b32_e32 v128, v128, v129, vcc
	v_rsq_f32_e32 v128, v128
	s_nop 0
	v_mul_f32_e32 v129, 0x45800000, v128
	v_cndmask_b32_e32 v128, v128, v129, vcc
	v_fma_f32 v132, v132, s39, v171
	v_mul_f32_e32 v133, 0x4b800000, v132
	v_cmp_gt_f32_e32 vcc, s40, v132
	s_nop 1
	v_cndmask_b32_e32 v132, v132, v133, vcc
	v_rsq_f32_e32 v132, v132
	s_nop 0
	v_mul_f32_e32 v133, 0x45800000, v132
	v_cndmask_b32_e32 v132, v132, v133, vcc
	v_fma_f32 v136, v136, s39, v171
	v_mul_f32_e32 v137, 0x4b800000, v136
	v_cmp_gt_f32_e32 vcc, s40, v136
	s_nop 1
	v_cndmask_b32_e32 v136, v136, v137, vcc
	v_rsq_f32_e32 v136, v136
	s_nop 0
	v_mul_f32_e32 v137, 0x45800000, v136
	v_cndmask_b32_e32 v136, v136, v137, vcc
	v_fma_f32 v252, v252, s39, v171
	v_mul_f32_e32 v253, 0x4b800000, v252
	v_cmp_gt_f32_e32 vcc, s40, v252
	s_nop 1
	v_cndmask_b32_e32 v252, v252, v253, vcc
	v_rsq_f32_e32 v252, v252
	s_nop 0
	v_mul_f32_e32 v253, 0x45800000, v252
	v_cndmask_b32_e32 v252, v252, v253, vcc
	v_pk_mul_f32 v[172:173], v[172:173], v[128:129] op_sel_hi:[1,0]
	v_pk_mul_f32 v[174:175], v[174:175], v[128:129] op_sel_hi:[1,0]
	v_pk_mul_f32 v[176:177], v[176:177], v[128:129] op_sel_hi:[1,0]
	v_pk_mul_f32 v[178:179], v[178:179], v[128:129] op_sel_hi:[1,0]
	v_pk_mul_f32 v[180:181], v[180:181], v[128:129] op_sel_hi:[1,0]
	v_pk_mul_f32 v[182:183], v[182:183], v[128:129] op_sel_hi:[1,0]
	v_pk_mul_f32 v[184:185], v[184:185], v[128:129] op_sel_hi:[1,0]
	v_pk_mul_f32 v[186:187], v[186:187], v[128:129] op_sel_hi:[1,0]
	v_pk_mul_f32 v[172:173], v[172:173], v[18:19]
	v_pk_mul_f32 v[174:175], v[174:175], v[20:21]
	v_pk_mul_f32 v[176:177], v[176:177], v[22:23]
	v_pk_mul_f32 v[178:179], v[178:179], v[24:25]
	v_pk_mul_f32 v[180:181], v[180:181], v[26:27]
	v_pk_mul_f32 v[182:183], v[182:183], v[28:29]
	v_pk_mul_f32 v[184:185], v[184:185], v[30:31]
	v_pk_mul_f32 v[186:187], v[186:187], v[32:33]
	s_add_u32 s34, s14, 0x2000000
	s_addc_u32 s35, s15, 0
	global_store_dwordx4 v3, v[172:175], s[34:35]
	global_store_dwordx4 v3, v[176:179], s[34:35] offset:1024
	global_store_dwordx4 v3, v[180:183], s[34:35] offset:2048
	global_store_dwordx4 v3, v[184:187], s[34:35] offset:3072
	v_pk_mul_f32 v[188:189], v[188:189], v[132:133] op_sel_hi:[1,0]
	v_pk_mul_f32 v[190:191], v[190:191], v[132:133] op_sel_hi:[1,0]
	v_pk_mul_f32 v[192:193], v[192:193], v[132:133] op_sel_hi:[1,0]
	v_pk_mul_f32 v[194:195], v[194:195], v[132:133] op_sel_hi:[1,0]
	v_pk_mul_f32 v[196:197], v[196:197], v[132:133] op_sel_hi:[1,0]
	v_pk_mul_f32 v[198:199], v[198:199], v[132:133] op_sel_hi:[1,0]
	v_pk_mul_f32 v[200:201], v[200:201], v[132:133] op_sel_hi:[1,0]
	v_pk_mul_f32 v[202:203], v[202:203], v[132:133] op_sel_hi:[1,0]
	v_pk_mul_f32 v[188:189], v[188:189], v[18:19]
	v_pk_mul_f32 v[190:191], v[190:191], v[20:21]
	v_pk_mul_f32 v[192:193], v[192:193], v[22:23]
	v_pk_mul_f32 v[194:195], v[194:195], v[24:25]
	v_pk_mul_f32 v[196:197], v[196:197], v[26:27]
	v_pk_mul_f32 v[198:199], v[198:199], v[28:29]
	v_pk_mul_f32 v[200:201], v[200:201], v[30:31]
	v_pk_mul_f32 v[202:203], v[202:203], v[32:33]
	s_add_u32 s34, s14, 0x2800000
	s_addc_u32 s35, s15, 0
	global_store_dwordx4 v3, v[188:191], s[34:35]
	global_store_dwordx4 v3, v[192:195], s[34:35] offset:1024
	global_store_dwordx4 v3, v[196:199], s[34:35] offset:2048
	global_store_dwordx4 v3, v[200:203], s[34:35] offset:3072
	v_pk_mul_f32 v[204:205], v[204:205], v[136:137] op_sel_hi:[1,0]
	v_pk_mul_f32 v[206:207], v[206:207], v[136:137] op_sel_hi:[1,0]
	v_pk_mul_f32 v[208:209], v[208:209], v[136:137] op_sel_hi:[1,0]
	v_pk_mul_f32 v[210:211], v[210:211], v[136:137] op_sel_hi:[1,0]
	v_pk_mul_f32 v[212:213], v[212:213], v[136:137] op_sel_hi:[1,0]
	v_pk_mul_f32 v[214:215], v[214:215], v[136:137] op_sel_hi:[1,0]
	v_pk_mul_f32 v[216:217], v[216:217], v[136:137] op_sel_hi:[1,0]
	v_pk_mul_f32 v[218:219], v[218:219], v[136:137] op_sel_hi:[1,0]
	v_pk_mul_f32 v[204:205], v[204:205], v[18:19]
	v_pk_mul_f32 v[206:207], v[206:207], v[20:21]
	v_pk_mul_f32 v[208:209], v[208:209], v[22:23]
	v_pk_mul_f32 v[210:211], v[210:211], v[24:25]
	v_pk_mul_f32 v[212:213], v[212:213], v[26:27]
	v_pk_mul_f32 v[214:215], v[214:215], v[28:29]
	v_pk_mul_f32 v[216:217], v[216:217], v[30:31]
	v_pk_mul_f32 v[218:219], v[218:219], v[32:33]
	s_add_u32 s34, s14, 0x3000000
	s_addc_u32 s35, s15, 0
	global_store_dwordx4 v3, v[204:207], s[34:35]
	global_store_dwordx4 v3, v[208:211], s[34:35] offset:1024
	global_store_dwordx4 v3, v[212:215], s[34:35] offset:2048
	global_store_dwordx4 v3, v[216:219], s[34:35] offset:3072
	v_pk_mul_f32 v[236:237], v[236:237], v[252:253] op_sel_hi:[1,0]
	v_pk_mul_f32 v[238:239], v[238:239], v[252:253] op_sel_hi:[1,0]
	v_pk_mul_f32 v[240:241], v[240:241], v[252:253] op_sel_hi:[1,0]
	v_pk_mul_f32 v[242:243], v[242:243], v[252:253] op_sel_hi:[1,0]
	v_pk_mul_f32 v[244:245], v[244:245], v[252:253] op_sel_hi:[1,0]
	v_pk_mul_f32 v[246:247], v[246:247], v[252:253] op_sel_hi:[1,0]
	v_pk_mul_f32 v[248:249], v[248:249], v[252:253] op_sel_hi:[1,0]
	v_pk_mul_f32 v[250:251], v[250:251], v[252:253] op_sel_hi:[1,0]
	v_pk_mul_f32 v[236:237], v[236:237], v[18:19]
	v_pk_mul_f32 v[238:239], v[238:239], v[20:21]
	v_pk_mul_f32 v[240:241], v[240:241], v[22:23]
	v_pk_mul_f32 v[242:243], v[242:243], v[24:25]
	v_pk_mul_f32 v[244:245], v[244:245], v[26:27]
	v_pk_mul_f32 v[246:247], v[246:247], v[28:29]
	v_pk_mul_f32 v[248:249], v[248:249], v[30:31]
	v_pk_mul_f32 v[250:251], v[250:251], v[32:33]
	s_add_u32 s34, s14, 0x3800000
	s_addc_u32 s35, s15, 0
	global_store_dwordx4 v3, v[236:239], s[34:35]
	global_store_dwordx4 v3, v[240:243], s[34:35] offset:1024
	global_store_dwordx4 v3, v[244:247], s[34:35] offset:2048
	global_store_dwordx4 v3, v[248:251], s[34:35] offset:3072
	s_branch .LBB0_2997
; DI void phase_final(const Args& A, int gw, int ngw, int lane) {
;     const bf16* xin = (const bf16*)(A.ws + WS_X1);
;     f32x4 gg[4];
; #pragma unroll
;     for (int j = 0; j < 4; ++j) gg[j] = ((const f32x4*)A.in[I_FG] + lane)[64 * j];
;     for (int tok = gw; tok < NT; tok += 2 * ngw) {
;         const int tokb = tok + ngw; const bool hb2 = tokb < NT;
;         f32x4 va[4], vb[4]; load_row_bf(xin + (size_t)tok * DM, lane, va); load_row_bf(xin + (size_t)(hb2 ? tokb : tok) * DM, lane, vb);
;         add_slots(A, tok, lane, va); add_slots(A, hb2 ? tokb : tok, lane, vb);
.Lrw2_orig:
	v_readlane_b32 s20, v235, 0
	v_lshlrev_b32_e32 v0, 4, v146
	v_readlane_b32 s24, v235, 4
	v_readlane_b32 s25, v235, 5
	s_nop 4
	global_load_dwordx4 v[80:83], v0, s[24:25]
	global_load_dwordx4 v[84:87], v0, s[24:25] offset:1024
	global_load_dwordx4 v[88:91], v0, s[24:25] offset:2048
	global_load_dwordx4 v[92:95], v0, s[24:25] offset:3072
	s_waitcnt vmcnt(0)
	v_mbcnt_lo_u32_b32 v2, -1, 0
	v_mbcnt_hi_u32_b32 v2, -1, v2
	v_and_b32_e32 v112, 64, v2
	v_xor_b32_e32 v3, 16, v2
	v_add_u32_e32 v4, 64, v112
	v_cmp_lt_i32_e32 vcc, v3, v4
	v_mov_b32_e32 v97, 0
	v_lshlrev_b32_e32 v96, 3, v146
	v_cndmask_b32_e32 v3, v2, v3, vcc
	v_lshlrev_b32_e32 v113, 2, v3
	v_xor_b32_e32 v3, 32, v2
	v_cmp_lt_i32_e32 vcc, v3, v4
	v_lshl_add_u64 v[0:1], s[4:5], 0, v[96:97]
	v_lshlrev_b32_e32 v96, 2, v146
	v_cndmask_b32_e32 v2, v2, v3, vcc
	v_lshlrev_b32_e32 v114, 2, v2
	v_lshl_add_u64 v[2:3], s[4:5], 0, v[96:97]
	s_mov_b64 s[2:3], 0x2c700000
	s_mov_b64 s[0:1], 0x22600000
	v_lshl_add_u64 v[100:101], v[2:3], 0, s[2:3]
	s_mov_b64 s[2:3], 0x3ba00000
	v_readlane_b32 s26, v235, 6
	v_readlane_b32 s27, v235, 7
	v_lshl_add_u64 v[98:99], v[0:1], 0, s[0:1]
	v_cmp_gt_u32_e64 s[0:1], 16, v146
	v_lshl_add_u64 v[102:103], v[0:1], 0, s[2:3]
	v_mov_b32_e32 v115, 0x358637bd
	s_mov_b32 s16, 0x800000
	v_readlane_b32 s24, v235, 56
	v_readlane_b32 s28, v235, 54
	v_readlane_b32 s21, v235, 1
	v_readlane_b32 s22, v235, 2
	v_readlane_b32 s23, v235, 3
	v_readlane_b32 s29, v235, 55
	s_branch .LBB0_2953
